# speedup vs baseline: 1.0142x; 1.0018x over previous
.LBB2_13:
	s_or_b64 exec, exec, s[10:11]
	v_cvt_f32_f16_e32 v89, v24
	v_cvt_f32_f16_e32 v49, v108
	v_lshlrev_b32_e32 v52, 3, v107
	s_movk_i32 s0, 0x50
	v_mad_u32_u24 v24, v136, s0, v52
	v_mad_u32_u24 v218, v135, s0, v52
	v_mov_b32_e32 v164, 0x3fb8aa3b
	v_mov_b32_e32 v165, 0x3fb8aa3b
	v_mov_b32_e32 v166, 0x3f317218
	v_mov_b32_e32 v167, 0x3f317218
	v_mov_b32_e32 v168, 1.0
	v_mov_b32_e32 v169, 1.0
	v_mov_b32_e32 v212, v134
	v_mov_b32_e32 v214, v133
	v_mov_b32_e32 v216, v131
	v_mov_b32_e32 v220, v121
	v_mfma_f32_16x16x32_f16 v[170:173], v[42:45], v[34:37], 0
	v_mfma_f32_16x16x32_f16 v[186:189], v[38:41], v[34:37], 0
	v_mfma_f32_16x16x32_f16 v[174:177], v[42:45], v[30:33], 0
	v_mfma_f32_16x16x32_f16 v[190:193], v[38:41], v[30:33], 0
	s_waitcnt vmcnt(9)
	v_mfma_f32_16x16x32_f16 v[178:181], v[42:45], v[26:29], 0
	v_mfma_f32_16x16x32_f16 v[194:197], v[38:41], v[26:29], 0
	s_waitcnt vmcnt(8)
	v_mfma_f32_16x16x32_f16 v[182:185], v[42:45], v[18:21], 0
	v_mfma_f32_16x16x32_f16 v[198:201], v[38:41], v[18:21], 0
	v_pk_add_f32 v[202:203], v[170:171], v[212:213] op_sel_hi:[1,0]
	v_pk_add_f32 v[204:205], v[172:173], v[212:213] op_sel_hi:[1,0]
	v_pk_add_f32 v[222:223], v[186:187], v[212:213] op_sel_hi:[1,0]
	v_pk_add_f32 v[224:225], v[188:189], v[212:213] op_sel_hi:[1,0]
	v_min_f32_e32 v206, 0x42a00000, v202
	v_min_f32_e32 v207, 0x42a00000, v203
	v_min_f32_e32 v208, 0x42a00000, v204
	v_min_f32_e32 v209, 0x42a00000, v205
	v_min_f32_e32 v226, 0x42a00000, v222
	v_min_f32_e32 v227, 0x42a00000, v223
	v_min_f32_e32 v228, 0x42a00000, v224
	v_min_f32_e32 v229, 0x42a00000, v225
	v_pk_mul_f32 v[206:207], v[206:207], v[164:165]
	v_pk_mul_f32 v[208:209], v[208:209], v[164:165]
	v_pk_mul_f32 v[226:227], v[226:227], v[164:165]
	v_pk_mul_f32 v[228:229], v[228:229], v[164:165]
	v_exp_f32_e32 v206, v206
	v_exp_f32_e32 v207, v207
	v_exp_f32_e32 v208, v208
	v_exp_f32_e32 v209, v209
	v_exp_f32_e32 v226, v226
	v_exp_f32_e32 v227, v227
	v_exp_f32_e32 v228, v228
	v_exp_f32_e32 v229, v229
	v_pk_add_f32 v[206:207], v[206:207], v[168:169]
	v_pk_add_f32 v[208:209], v[208:209], v[168:169]
	v_pk_add_f32 v[226:227], v[226:227], v[168:169]
	v_pk_add_f32 v[228:229], v[228:229], v[168:169]
	v_log_f32_e32 v206, v206
	v_log_f32_e32 v207, v207
	v_log_f32_e32 v208, v208
	v_log_f32_e32 v209, v209
	v_log_f32_e32 v226, v226
	v_log_f32_e32 v227, v227
	v_log_f32_e32 v228, v228
	v_log_f32_e32 v229, v229
	v_pk_mul_f32 v[206:207], v[206:207], v[166:167]
	v_pk_mul_f32 v[208:209], v[208:209], v[166:167]
	v_pk_mul_f32 v[226:227], v[226:227], v[166:167]
	v_pk_mul_f32 v[228:229], v[228:229], v[166:167]
	v_max_f32_e32 v202, v202, v206
	v_max_f32_e32 v203, v203, v207
	v_max_f32_e32 v204, v204, v208
	v_max_f32_e32 v205, v205, v209
	v_max_f32_e32 v222, v222, v226
	v_max_f32_e32 v223, v223, v227
	v_max_f32_e32 v224, v224, v228
	v_max_f32_e32 v225, v225, v229
	v_cvt_pk_f16_f32 v210, v202, v203
	v_cvt_pk_f16_f32 v211, v204, v205
	v_cvt_pk_f16_f32 v230, v222, v223
	v_cvt_pk_f16_f32 v231, v224, v225
	ds_write_b64 v24, v[210:211]
	ds_write_b64 v24, v[230:231] offset:32
	v_pk_add_f32 v[202:203], v[174:175], v[214:215] op_sel_hi:[1,0]
	v_pk_add_f32 v[204:205], v[176:177], v[214:215] op_sel_hi:[1,0]
	v_pk_add_f32 v[222:223], v[190:191], v[214:215] op_sel_hi:[1,0]
	v_pk_add_f32 v[224:225], v[192:193], v[214:215] op_sel_hi:[1,0]
	v_min_f32_e32 v206, 0x42a00000, v202
	v_min_f32_e32 v207, 0x42a00000, v203
	v_min_f32_e32 v208, 0x42a00000, v204
	v_min_f32_e32 v209, 0x42a00000, v205
	v_min_f32_e32 v226, 0x42a00000, v222
	v_min_f32_e32 v227, 0x42a00000, v223
	v_min_f32_e32 v228, 0x42a00000, v224
	v_min_f32_e32 v229, 0x42a00000, v225
	v_pk_mul_f32 v[206:207], v[206:207], v[164:165]
	v_pk_mul_f32 v[208:209], v[208:209], v[164:165]
	v_pk_mul_f32 v[226:227], v[226:227], v[164:165]
	v_pk_mul_f32 v[228:229], v[228:229], v[164:165]
	v_exp_f32_e32 v206, v206
	v_exp_f32_e32 v207, v207
	v_exp_f32_e32 v208, v208
	v_exp_f32_e32 v209, v209
	v_exp_f32_e32 v226, v226
	v_exp_f32_e32 v227, v227
	v_exp_f32_e32 v228, v228
	v_exp_f32_e32 v229, v229
	v_pk_add_f32 v[206:207], v[206:207], v[168:169]
	v_pk_add_f32 v[208:209], v[208:209], v[168:169]
	v_pk_add_f32 v[226:227], v[226:227], v[168:169]
	v_pk_add_f32 v[228:229], v[228:229], v[168:169]
	v_log_f32_e32 v206, v206
	v_log_f32_e32 v207, v207
	v_log_f32_e32 v208, v208
	v_log_f32_e32 v209, v209
	v_log_f32_e32 v226, v226
	v_log_f32_e32 v227, v227
	v_log_f32_e32 v228, v228
	v_log_f32_e32 v229, v229
	v_pk_mul_f32 v[206:207], v[206:207], v[166:167]
	v_pk_mul_f32 v[208:209], v[208:209], v[166:167]
	v_pk_mul_f32 v[226:227], v[226:227], v[166:167]
	v_pk_mul_f32 v[228:229], v[228:229], v[166:167]
	v_max_f32_e32 v202, v202, v206
	v_max_f32_e32 v203, v203, v207
	v_max_f32_e32 v204, v204, v208
	v_max_f32_e32 v205, v205, v209
	v_max_f32_e32 v222, v222, v226
	v_max_f32_e32 v223, v223, v227
	v_max_f32_e32 v224, v224, v228
	v_max_f32_e32 v225, v225, v229
	v_cvt_pk_f16_f32 v210, v202, v203
	v_cvt_pk_f16_f32 v211, v204, v205
	v_cvt_pk_f16_f32 v230, v222, v223
	v_cvt_pk_f16_f32 v231, v224, v225
	ds_write_b64 v24, v[210:211] offset:1280
	ds_write_b64 v24, v[230:231] offset:1312
	v_pk_add_f32 v[202:203], v[178:179], v[216:217] op_sel_hi:[1,0]
	v_pk_add_f32 v[204:205], v[180:181], v[216:217] op_sel_hi:[1,0]
	v_pk_add_f32 v[222:223], v[194:195], v[216:217] op_sel_hi:[1,0]
	v_pk_add_f32 v[224:225], v[196:197], v[216:217] op_sel_hi:[1,0]
	v_min_f32_e32 v206, 0x42a00000, v202
	v_min_f32_e32 v207, 0x42a00000, v203
	v_min_f32_e32 v208, 0x42a00000, v204
	v_min_f32_e32 v209, 0x42a00000, v205
	v_min_f32_e32 v226, 0x42a00000, v222
	v_min_f32_e32 v227, 0x42a00000, v223
	v_min_f32_e32 v228, 0x42a00000, v224
	v_min_f32_e32 v229, 0x42a00000, v225
	v_pk_mul_f32 v[206:207], v[206:207], v[164:165]
	v_pk_mul_f32 v[208:209], v[208:209], v[164:165]
	v_pk_mul_f32 v[226:227], v[226:227], v[164:165]
	v_pk_mul_f32 v[228:229], v[228:229], v[164:165]
	v_exp_f32_e32 v206, v206
	v_exp_f32_e32 v207, v207
	v_exp_f32_e32 v208, v208
	v_exp_f32_e32 v209, v209
	v_exp_f32_e32 v226, v226
	v_exp_f32_e32 v227, v227
	v_exp_f32_e32 v228, v228
	v_exp_f32_e32 v229, v229
	v_pk_add_f32 v[206:207], v[206:207], v[168:169]
	v_pk_add_f32 v[208:209], v[208:209], v[168:169]
	v_pk_add_f32 v[226:227], v[226:227], v[168:169]
	v_pk_add_f32 v[228:229], v[228:229], v[168:169]
	v_log_f32_e32 v206, v206
	v_log_f32_e32 v207, v207
	v_log_f32_e32 v208, v208
	v_log_f32_e32 v209, v209
	v_log_f32_e32 v226, v226
	v_log_f32_e32 v227, v227
	v_log_f32_e32 v228, v228
	v_log_f32_e32 v229, v229
	v_pk_mul_f32 v[206:207], v[206:207], v[166:167]
	v_pk_mul_f32 v[208:209], v[208:209], v[166:167]
	v_pk_mul_f32 v[226:227], v[226:227], v[166:167]
	v_pk_mul_f32 v[228:229], v[228:229], v[166:167]
	v_max_f32_e32 v202, v202, v206
	v_max_f32_e32 v203, v203, v207
	v_max_f32_e32 v204, v204, v208
	v_max_f32_e32 v205, v205, v209
	v_max_f32_e32 v222, v222, v226
	v_max_f32_e32 v223, v223, v227
	v_max_f32_e32 v224, v224, v228
	v_max_f32_e32 v225, v225, v229
	v_cvt_pk_f16_f32 v210, v202, v203
	v_cvt_pk_f16_f32 v211, v204, v205
	v_cvt_pk_f16_f32 v230, v222, v223
	v_cvt_pk_f16_f32 v231, v224, v225
	ds_write_b64 v24, v[210:211] offset:2560
	ds_write_b64 v24, v[230:231] offset:2592
	v_pk_add_f32 v[202:203], v[182:183], v[220:221] op_sel_hi:[1,0]
	v_pk_add_f32 v[204:205], v[184:185], v[220:221] op_sel_hi:[1,0]
	v_pk_add_f32 v[222:223], v[198:199], v[220:221] op_sel_hi:[1,0]
	v_pk_add_f32 v[224:225], v[200:201], v[220:221] op_sel_hi:[1,0]
	v_min_f32_e32 v206, 0x42a00000, v202
	v_min_f32_e32 v207, 0x42a00000, v203
	v_min_f32_e32 v208, 0x42a00000, v204
	v_min_f32_e32 v209, 0x42a00000, v205
	v_min_f32_e32 v226, 0x42a00000, v222
	v_min_f32_e32 v227, 0x42a00000, v223
	v_min_f32_e32 v228, 0x42a00000, v224
	v_min_f32_e32 v229, 0x42a00000, v225
	v_pk_mul_f32 v[206:207], v[206:207], v[164:165]
	v_pk_mul_f32 v[208:209], v[208:209], v[164:165]
	v_pk_mul_f32 v[226:227], v[226:227], v[164:165]
	v_pk_mul_f32 v[228:229], v[228:229], v[164:165]
	v_exp_f32_e32 v206, v206
	v_exp_f32_e32 v207, v207
	v_exp_f32_e32 v208, v208
	v_exp_f32_e32 v209, v209
	v_exp_f32_e32 v226, v226
	v_exp_f32_e32 v227, v227
	v_exp_f32_e32 v228, v228
	v_exp_f32_e32 v229, v229
	v_pk_add_f32 v[206:207], v[206:207], v[168:169]
	v_pk_add_f32 v[208:209], v[208:209], v[168:169]
	v_pk_add_f32 v[226:227], v[226:227], v[168:169]
	v_pk_add_f32 v[228:229], v[228:229], v[168:169]
	v_log_f32_e32 v206, v206
	v_log_f32_e32 v207, v207
	v_log_f32_e32 v208, v208
	v_log_f32_e32 v209, v209
	v_log_f32_e32 v226, v226
	v_log_f32_e32 v227, v227
	v_log_f32_e32 v228, v228
	v_log_f32_e32 v229, v229
	v_pk_mul_f32 v[206:207], v[206:207], v[166:167]
	v_pk_mul_f32 v[208:209], v[208:209], v[166:167]
	v_pk_mul_f32 v[226:227], v[226:227], v[166:167]
	v_pk_mul_f32 v[228:229], v[228:229], v[166:167]
	v_max_f32_e32 v202, v202, v206
	v_max_f32_e32 v203, v203, v207
	v_max_f32_e32 v204, v204, v208
	v_max_f32_e32 v205, v205, v209
	v_max_f32_e32 v222, v222, v226
	v_max_f32_e32 v223, v223, v227
	v_max_f32_e32 v224, v224, v228
	v_max_f32_e32 v225, v225, v229
	v_cvt_pk_f16_f32 v210, v202, v203
	v_cvt_pk_f16_f32 v211, v204, v205
	v_cvt_pk_f16_f32 v230, v222, v223
	v_cvt_pk_f16_f32 v231, v224, v225
	ds_write_b64 v218, v[210:211]
	ds_write_b64 v218, v[230:231] offset:32
	v_mul_u32_u24_e32 v18, 0x50, v0
	s_waitcnt lgkmcnt(0)
	s_barrier
	ds_read_b128 v[92:95], v18
	v_cvt_f32_f16_e32 v55, v111
	v_cvt_f32_f16_e32 v59, v110
	v_cvt_f32_f16_e32 v79, v105
	v_cvt_f32_f16_e32 v82, v104
	v_cvt_f32_f16_e32 v84, v103
	v_cvt_f32_f16_e32 v86, v102
	ds_read_b128 v[96:99], v18 offset:16
	ds_read_b128 v[100:103], v18 offset:32
	ds_read_b128 v[108:111], v18 offset:48
	v_lshl_add_u64 v[104:105], s[8:9], 0, v[118:119]
	v_cvt_f32_f16_e32 v47, v113
	v_cvt_f32_f16_e32 v51, v112
	v_lshl_add_u64 v[112:113], v[104:105], 0, s[6:7]
	s_waitcnt lgkmcnt(3)
	v_cvt_f32_f16_e32 v26, v94
	v_cvt_f32_f16_sdwa v28, v94 dst_sel:DWORD dst_unused:UNUSED_PAD src0_sel:WORD_1
	v_cvt_f32_f16_e32 v30, v95
	v_cvt_f32_f16_sdwa v32, v95 dst_sel:DWORD dst_unused:UNUSED_PAD src0_sel:WORD_1
	global_store_dwordx4 v[112:113], v[92:95], off sc0 sc1
	v_cvt_f32_f16_e32 v53, v122
	v_cvt_f32_f16_e32 v57, v125
	v_lshl_add_u64 v[94:95], v[104:105], 0, s[14:15]
	s_waitcnt lgkmcnt(2)
	global_store_dwordx4 v[94:95], v[96:99], off sc0 sc1
	v_lshl_add_u64 v[94:95], v[104:105], 0, s[16:17]
	s_waitcnt lgkmcnt(1)
	global_store_dwordx4 v[94:95], v[100:103], off sc0 sc1
	v_lshl_add_u64 v[94:95], v[104:105], 0, s[18:19]
	v_cvt_f32_f16_e32 v61, v124
	v_cvt_f32_f16_e32 v63, v117
	v_cvt_f32_f16_e32 v65, v147
	v_cvt_f32_f16_e32 v67, v116
	v_cvt_f32_f16_e32 v69, v145
	v_cvt_f32_f16_e32 v71, v115
	v_cvt_f32_f16_e32 v73, v127
	v_cvt_f32_f16_e32 v75, v114
	v_cvt_f32_f16_e32 v77, v126
	v_cvt_f32_f16_e32 v81, v142
	v_cvt_f32_f16_e32 v83, v141
	v_cvt_f32_f16_e32 v85, v140
	v_cvt_f32_f16_e32 v87, v139
	v_cvt_f32_f16_e32 v25, v25
	v_cvt_f32_f16_e32 v88, v138
	v_cvt_f32_f16_e32 v90, v137
	v_cvt_f32_f16_e32 v23, v23
	v_cvt_f32_f16_e32 v91, v123
	v_cvt_f32_f16_e32 v19, v22
	v_cvt_f32_f16_sdwa v20, v92 dst_sel:DWORD dst_unused:UNUSED_PAD src0_sel:WORD_1
	v_cvt_f32_f16_e32 v22, v93
	v_cvt_f32_f16_sdwa v24, v93 dst_sel:DWORD dst_unused:UNUSED_PAD src0_sel:WORD_1
	v_cvt_f32_f16_e32 v34, v96
	v_cvt_f32_f16_sdwa v36, v96 dst_sel:DWORD dst_unused:UNUSED_PAD src0_sel:WORD_1
	v_cvt_f32_f16_e32 v38, v97
	v_cvt_f32_f16_sdwa v40, v97 dst_sel:DWORD dst_unused:UNUSED_PAD src0_sel:WORD_1
	v_cvt_f32_f16_e32 v42, v98
	v_cvt_f32_f16_sdwa v44, v98 dst_sel:DWORD dst_unused:UNUSED_PAD src0_sel:WORD_1
	v_cvt_f32_f16_e32 v46, v99
	v_cvt_f32_f16_sdwa v48, v99 dst_sel:DWORD dst_unused:UNUSED_PAD src0_sel:WORD_1
	v_cvt_f32_f16_e32 v50, v100
	v_cvt_f32_f16_sdwa v52, v100 dst_sel:DWORD dst_unused:UNUSED_PAD src0_sel:WORD_1
	v_cvt_f32_f16_e32 v54, v101
	v_cvt_f32_f16_sdwa v56, v101 dst_sel:DWORD dst_unused:UNUSED_PAD src0_sel:WORD_1
	v_cvt_f32_f16_e32 v58, v102
	v_cvt_f32_f16_sdwa v60, v102 dst_sel:DWORD dst_unused:UNUSED_PAD src0_sel:WORD_1
	v_cvt_f32_f16_e32 v62, v103
	v_cvt_f32_f16_sdwa v64, v103 dst_sel:DWORD dst_unused:UNUSED_PAD src0_sel:WORD_1
	s_waitcnt lgkmcnt(0)
	v_cvt_f32_f16_e32 v66, v108
	v_cvt_f32_f16_sdwa v68, v108 dst_sel:DWORD dst_unused:UNUSED_PAD src0_sel:WORD_1
	v_cvt_f32_f16_e32 v70, v109
	v_cvt_f32_f16_sdwa v72, v109 dst_sel:DWORD dst_unused:UNUSED_PAD src0_sel:WORD_1
	v_cvt_f32_f16_e32 v74, v110
	v_cvt_f32_f16_sdwa v76, v110 dst_sel:DWORD dst_unused:UNUSED_PAD src0_sel:WORD_1
	v_cvt_f32_f16_e32 v78, v111
	v_cvt_f32_f16_sdwa v18, v111 dst_sel:DWORD dst_unused:UNUSED_PAD src0_sel:WORD_1
	global_store_dwordx4 v[94:95], v[108:111], off sc0 sc1
	v_cvt_f32_f16_e32 v80, v92
	v_mov_b32_e32 v160, 0
	ds_read_b128 v[92:95], v160 offset:41024
	ds_read_b128 v[96:99], v160 offset:41040
	ds_read_b128 v[100:103], v160 offset:41056
	ds_read_b128 v[108:111], v160 offset:41072
	s_waitcnt lgkmcnt(0)
	ds_read_b128 v[112:115], v160 offset:41232
	ds_read_b128 v[116:119], v160 offset:41248
	ds_read_b128 v[120:123], v160 offset:41264
	ds_read_b128 v[124:127], v160 offset:41280
	s_lshr_b32 s0, s23, 5
	s_waitcnt vmcnt(11)
	v_mul_f32_e32 v104, v80, v19
	v_pk_mul_f32 v[128:129], v[104:105], v[92:93] op_sel_hi:[0,1]
	v_pk_mul_f32 v[130:131], v[104:105], v[94:95] op_sel_hi:[0,1]
	s_waitcnt vmcnt(10)
	v_pk_mul_f32 v[132:133], v[104:105], v[96:97] op_sel_hi:[0,1]
	v_pk_mul_f32 v[134:135], v[104:105], v[98:99] op_sel_hi:[0,1]
	s_waitcnt vmcnt(9)
	v_pk_mul_f32 v[136:137], v[104:105], v[100:101] op_sel_hi:[0,1]
	v_pk_mul_f32 v[138:139], v[104:105], v[102:103] op_sel_hi:[0,1]
	s_waitcnt vmcnt(8)
	v_pk_mul_f32 v[140:141], v[104:105], v[108:109] op_sel_hi:[0,1]
	v_pk_mul_f32 v[104:105], v[104:105], v[110:111] op_sel_hi:[0,1]
	s_waitcnt lgkmcnt(0)
	s_and_b32 s6, s22, 0x7ffffc0
	ds_read_b128 v[92:95], v160 offset:41440
	ds_read_b128 v[96:99], v160 offset:41456
	ds_read_b128 v[100:103], v160 offset:41472
	ds_read_b128 v[108:111], v160 offset:41488
	v_pk_mul_f32 v[142:143], v[20:21], v[14:15] op_sel_hi:[0,1]
	v_exp_f32_e32 v142, v142
	v_exp_f32_e32 v143, v143
	v_mul_f32_e32 v144, v20, v91
	v_pk_mul_f32 v[112:113], v[144:145], v[112:113] op_sel_hi:[0,1]
	v_pk_mul_f32 v[114:115], v[144:145], v[114:115] op_sel_hi:[0,1]
	v_pk_fma_f32 v[128:129], v[128:129], v[142:143], v[112:113]
	v_pk_mul_f32 v[112:113], v[20:21], v[16:17] op_sel_hi:[0,1]
	v_exp_f32_e32 v112, v112
	v_exp_f32_e32 v113, v113
	v_pk_mul_f32 v[116:117], v[144:145], v[116:117] op_sel_hi:[0,1]
	s_or_b32 s0, s0, s6
	s_lshl_b64 s[6:7], s[0:1], 14
	v_pk_fma_f32 v[130:131], v[130:131], v[112:113], v[114:115]
	v_pk_mul_f32 v[112:113], v[20:21], v[10:11] op_sel_hi:[0,1]
	v_exp_f32_e32 v112, v112
	v_exp_f32_e32 v113, v113
	v_pk_mul_f32 v[114:115], v[20:21], v[12:13] op_sel_hi:[0,1]
	v_exp_f32_e32 v114, v114
	v_exp_f32_e32 v115, v115
	v_pk_fma_f32 v[132:133], v[132:133], v[112:113], v[116:117]
	v_pk_mul_f32 v[112:113], v[144:145], v[118:119] op_sel_hi:[0,1]
	v_pk_mul_f32 v[116:117], v[144:145], v[120:121] op_sel_hi:[0,1]
	v_pk_fma_f32 v[134:135], v[134:135], v[114:115], v[112:113]
	v_pk_mul_f32 v[112:113], v[20:21], v[6:7] op_sel_hi:[0,1]
	v_exp_f32_e32 v112, v112
	v_exp_f32_e32 v113, v113
	v_pk_mul_f32 v[114:115], v[20:21], v[8:9] op_sel_hi:[0,1]
	v_exp_f32_e32 v114, v114
	v_exp_f32_e32 v115, v115
	v_pk_fma_f32 v[136:137], v[136:137], v[112:113], v[116:117]
	v_pk_mul_f32 v[112:113], v[144:145], v[122:123] op_sel_hi:[0,1]
	v_pk_mul_f32 v[116:117], v[144:145], v[124:125] op_sel_hi:[0,1]
	v_pk_fma_f32 v[138:139], v[138:139], v[114:115], v[112:113]
	v_pk_mul_f32 v[112:113], v[20:21], v[2:3] op_sel_hi:[0,1]
	v_exp_f32_e32 v112, v112
	v_exp_f32_e32 v113, v113
	v_pk_mul_f32 v[114:115], v[20:21], v[4:5] op_sel_hi:[0,1]
	v_exp_f32_e32 v114, v114
	v_exp_f32_e32 v115, v115
	v_pk_fma_f32 v[140:141], v[140:141], v[112:113], v[116:117]
	v_pk_mul_f32 v[112:113], v[144:145], v[126:127] op_sel_hi:[0,1]
	s_lshl_b64 s[0:1], s[0:1], 11
	v_pk_fma_f32 v[104:105], v[104:105], v[114:115], v[112:113]
	s_add_u32 s0, s2, s0
	s_waitcnt lgkmcnt(0)
	s_addc_u32 s1, s3, s1
	ds_read_b128 v[112:115], v160 offset:41648
	ds_read_b128 v[116:119], v160 offset:41664
	ds_read_b128 v[120:123], v160 offset:41680
	ds_read_b128 v[124:127], v160 offset:41696
	v_pk_mul_f32 v[142:143], v[22:23], v[14:15] op_sel_hi:[0,1]
	v_exp_f32_e32 v142, v142
	v_exp_f32_e32 v143, v143
	v_mul_f32_e32 v144, v22, v23
	v_pk_mul_f32 v[92:93], v[144:145], v[92:93] op_sel_hi:[0,1]
	v_pk_mul_f32 v[94:95], v[144:145], v[94:95] op_sel_hi:[0,1]
	v_pk_fma_f32 v[128:129], v[128:129], v[142:143], v[92:93]
	v_pk_mul_f32 v[92:93], v[22:23], v[16:17] op_sel_hi:[0,1]
	v_exp_f32_e32 v92, v92
	v_exp_f32_e32 v93, v93
	v_pk_mul_f32 v[96:97], v[144:145], v[96:97] op_sel_hi:[0,1]
	v_pk_fma_f32 v[130:131], v[130:131], v[92:93], v[94:95]
	v_pk_mul_f32 v[92:93], v[22:23], v[10:11] op_sel_hi:[0,1]
	v_exp_f32_e32 v92, v92
	v_exp_f32_e32 v93, v93
	v_pk_mul_f32 v[94:95], v[22:23], v[12:13] op_sel_hi:[0,1]
	v_exp_f32_e32 v94, v94
	v_exp_f32_e32 v95, v95
	v_pk_fma_f32 v[132:133], v[132:133], v[92:93], v[96:97]
	v_pk_mul_f32 v[92:93], v[144:145], v[98:99] op_sel_hi:[0,1]
	v_pk_mul_f32 v[96:97], v[144:145], v[100:101] op_sel_hi:[0,1]
	v_pk_fma_f32 v[134:135], v[134:135], v[94:95], v[92:93]
	v_pk_mul_f32 v[92:93], v[22:23], v[6:7] op_sel_hi:[0,1]
	v_exp_f32_e32 v92, v92
	v_exp_f32_e32 v93, v93
	v_pk_mul_f32 v[94:95], v[22:23], v[8:9] op_sel_hi:[0,1]
	v_exp_f32_e32 v94, v94
	v_exp_f32_e32 v95, v95
	v_pk_fma_f32 v[136:137], v[136:137], v[92:93], v[96:97]
	v_pk_mul_f32 v[92:93], v[144:145], v[102:103] op_sel_hi:[0,1]
	v_pk_mul_f32 v[96:97], v[144:145], v[108:109] op_sel_hi:[0,1]
	v_pk_fma_f32 v[138:139], v[138:139], v[94:95], v[92:93]
	v_pk_mul_f32 v[92:93], v[22:23], v[2:3] op_sel_hi:[0,1]
	v_exp_f32_e32 v92, v92
	v_exp_f32_e32 v93, v93
	v_pk_mul_f32 v[94:95], v[22:23], v[4:5] op_sel_hi:[0,1]
	v_exp_f32_e32 v94, v94
	v_exp_f32_e32 v95, v95
	v_pk_fma_f32 v[140:141], v[140:141], v[92:93], v[96:97]
	v_pk_mul_f32 v[92:93], v[144:145], v[110:111] op_sel_hi:[0,1]
	v_pk_fma_f32 v[104:105], v[104:105], v[94:95], v[92:93]
	s_nop 0
	s_waitcnt lgkmcnt(0)
	s_nop 0
	ds_read_b128 v[92:95], v160 offset:41856
	ds_read_b128 v[96:99], v160 offset:41872
	ds_read_b128 v[100:103], v160 offset:41888
	ds_read_b128 v[108:111], v160 offset:41904
	v_pk_mul_f32 v[142:143], v[24:25], v[14:15] op_sel_hi:[0,1]
	v_exp_f32_e32 v142, v142
	v_exp_f32_e32 v143, v143
	v_mul_f32_e32 v90, v24, v90
	v_pk_mul_f32 v[112:113], v[90:91], v[112:113] op_sel_hi:[0,1]
	v_pk_mul_f32 v[114:115], v[90:91], v[114:115] op_sel_hi:[0,1]
	v_pk_fma_f32 v[128:129], v[128:129], v[142:143], v[112:113]
	v_pk_mul_f32 v[112:113], v[24:25], v[16:17] op_sel_hi:[0,1]
	v_exp_f32_e32 v112, v112
	v_exp_f32_e32 v113, v113
	v_pk_mul_f32 v[116:117], v[90:91], v[116:117] op_sel_hi:[0,1]
	v_pk_fma_f32 v[130:131], v[130:131], v[112:113], v[114:115]
	v_pk_mul_f32 v[112:113], v[24:25], v[10:11] op_sel_hi:[0,1]
	v_exp_f32_e32 v112, v112
	v_exp_f32_e32 v113, v113
	v_pk_mul_f32 v[114:115], v[24:25], v[12:13] op_sel_hi:[0,1]
	v_exp_f32_e32 v114, v114
	v_exp_f32_e32 v115, v115
	v_pk_fma_f32 v[132:133], v[132:133], v[112:113], v[116:117]
	v_pk_mul_f32 v[112:113], v[90:91], v[118:119] op_sel_hi:[0,1]
	v_pk_mul_f32 v[116:117], v[90:91], v[120:121] op_sel_hi:[0,1]
	v_pk_fma_f32 v[134:135], v[134:135], v[114:115], v[112:113]
	v_pk_mul_f32 v[112:113], v[24:25], v[6:7] op_sel_hi:[0,1]
	v_exp_f32_e32 v112, v112
	v_exp_f32_e32 v113, v113
	v_pk_mul_f32 v[114:115], v[24:25], v[8:9] op_sel_hi:[0,1]
	v_exp_f32_e32 v114, v114
	v_exp_f32_e32 v115, v115
	v_pk_fma_f32 v[136:137], v[136:137], v[112:113], v[116:117]
	v_pk_mul_f32 v[112:113], v[90:91], v[122:123] op_sel_hi:[0,1]
	v_pk_mul_f32 v[116:117], v[90:91], v[124:125] op_sel_hi:[0,1]
	v_pk_fma_f32 v[138:139], v[138:139], v[114:115], v[112:113]
	v_pk_mul_f32 v[112:113], v[24:25], v[2:3] op_sel_hi:[0,1]
	v_pk_mul_f32 v[114:115], v[24:25], v[4:5] op_sel_hi:[0,1]
	v_exp_f32_e32 v112, v112
	v_exp_f32_e32 v113, v113
	v_exp_f32_e32 v114, v114
	v_exp_f32_e32 v115, v115
	v_pk_mul_f32 v[90:91], v[90:91], v[126:127] op_sel_hi:[0,1]
	v_pk_fma_f32 v[140:141], v[140:141], v[112:113], v[116:117]
	v_pk_fma_f32 v[90:91], v[104:105], v[114:115], v[90:91]
	s_nop 0
	s_waitcnt lgkmcnt(0)
	s_nop 0
	ds_read_b128 v[112:115], v160 offset:42064
	ds_read_b128 v[116:119], v160 offset:42080
	ds_read_b128 v[120:123], v160 offset:42096
	ds_read_b128 v[124:127], v160 offset:42112
	v_pk_mul_f32 v[104:105], v[26:27], v[14:15] op_sel_hi:[0,1]
	v_exp_f32_e32 v104, v104
	v_exp_f32_e32 v105, v105
	v_mul_f32_e32 v142, v26, v89
	v_pk_mul_f32 v[92:93], v[142:143], v[92:93] op_sel_hi:[0,1]
	v_pk_mul_f32 v[94:95], v[142:143], v[94:95] op_sel_hi:[0,1]
	v_pk_fma_f32 v[128:129], v[128:129], v[104:105], v[92:93]
	v_pk_mul_f32 v[92:93], v[26:27], v[16:17] op_sel_hi:[0,1]
	v_exp_f32_e32 v92, v92
	v_exp_f32_e32 v93, v93
	v_pk_mul_f32 v[96:97], v[142:143], v[96:97] op_sel_hi:[0,1]
	v_pk_fma_f32 v[130:131], v[130:131], v[92:93], v[94:95]
	v_pk_mul_f32 v[92:93], v[26:27], v[10:11] op_sel_hi:[0,1]
	v_exp_f32_e32 v92, v92
	v_exp_f32_e32 v93, v93
	v_pk_mul_f32 v[94:95], v[26:27], v[12:13] op_sel_hi:[0,1]
	v_exp_f32_e32 v94, v94
	v_exp_f32_e32 v95, v95
	v_pk_fma_f32 v[132:133], v[132:133], v[92:93], v[96:97]
	v_pk_mul_f32 v[92:93], v[142:143], v[98:99] op_sel_hi:[0,1]
	v_pk_mul_f32 v[96:97], v[142:143], v[100:101] op_sel_hi:[0,1]
	v_pk_fma_f32 v[134:135], v[134:135], v[94:95], v[92:93]
	v_pk_mul_f32 v[92:93], v[26:27], v[6:7] op_sel_hi:[0,1]
	v_exp_f32_e32 v92, v92
	v_exp_f32_e32 v93, v93
	v_pk_mul_f32 v[94:95], v[26:27], v[8:9] op_sel_hi:[0,1]
	v_exp_f32_e32 v94, v94
	v_exp_f32_e32 v95, v95
	v_pk_fma_f32 v[136:137], v[136:137], v[92:93], v[96:97]
	v_pk_mul_f32 v[92:93], v[142:143], v[102:103] op_sel_hi:[0,1]
	v_pk_mul_f32 v[96:97], v[142:143], v[108:109] op_sel_hi:[0,1]
	v_pk_fma_f32 v[138:139], v[138:139], v[94:95], v[92:93]
	v_pk_mul_f32 v[92:93], v[26:27], v[2:3] op_sel_hi:[0,1]
	v_exp_f32_e32 v92, v92
	v_exp_f32_e32 v93, v93
	v_pk_mul_f32 v[94:95], v[26:27], v[4:5] op_sel_hi:[0,1]
	v_exp_f32_e32 v94, v94
	v_exp_f32_e32 v95, v95
	v_pk_fma_f32 v[108:109], v[140:141], v[92:93], v[96:97]
	v_pk_mul_f32 v[92:93], v[142:143], v[110:111] op_sel_hi:[0,1]
	v_pk_fma_f32 v[110:111], v[90:91], v[94:95], v[92:93]
	s_nop 0
	s_waitcnt lgkmcnt(0)
	s_nop 0
	ds_read_b128 v[90:93], v160 offset:42272
	ds_read_b128 v[94:97], v160 offset:42288
	ds_read_b128 v[98:101], v160 offset:42304
	ds_read_b128 v[102:105], v160 offset:42320
	v_pk_mul_f32 v[140:141], v[28:29], v[14:15] op_sel_hi:[0,1]
	v_exp_f32_e32 v140, v140
	v_exp_f32_e32 v141, v141
	v_pk_mul_f32 v[142:143], v[28:29], v[16:17] op_sel_hi:[0,1]
	v_exp_f32_e32 v142, v142
	v_exp_f32_e32 v143, v143
	v_mul_f32_e32 v88, v28, v88
	v_pk_mul_f32 v[112:113], v[88:89], v[112:113] op_sel_hi:[0,1]
	v_pk_fma_f32 v[128:129], v[128:129], v[140:141], v[112:113]
	v_pk_mul_f32 v[112:113], v[88:89], v[114:115] op_sel_hi:[0,1]
	v_pk_fma_f32 v[130:131], v[130:131], v[142:143], v[112:113]
	v_pk_mul_f32 v[112:113], v[28:29], v[10:11] op_sel_hi:[0,1]
	v_exp_f32_e32 v112, v112
	v_exp_f32_e32 v113, v113
	v_pk_mul_f32 v[114:115], v[28:29], v[12:13] op_sel_hi:[0,1]
	v_exp_f32_e32 v114, v114
	v_exp_f32_e32 v115, v115
	v_pk_mul_f32 v[116:117], v[88:89], v[116:117] op_sel_hi:[0,1]
	v_pk_fma_f32 v[132:133], v[132:133], v[112:113], v[116:117]
	v_pk_mul_f32 v[112:113], v[88:89], v[118:119] op_sel_hi:[0,1]
	v_pk_fma_f32 v[134:135], v[134:135], v[114:115], v[112:113]
	v_pk_mul_f32 v[112:113], v[28:29], v[6:7] op_sel_hi:[0,1]
	v_exp_f32_e32 v112, v112
	v_exp_f32_e32 v113, v113
	v_pk_mul_f32 v[114:115], v[28:29], v[8:9] op_sel_hi:[0,1]
	v_exp_f32_e32 v114, v114
	v_exp_f32_e32 v115, v115
	v_pk_mul_f32 v[116:117], v[88:89], v[120:121] op_sel_hi:[0,1]
	v_pk_fma_f32 v[136:137], v[136:137], v[112:113], v[116:117]
	v_pk_mul_f32 v[112:113], v[88:89], v[122:123] op_sel_hi:[0,1]
	v_pk_fma_f32 v[138:139], v[138:139], v[114:115], v[112:113]
	v_pk_mul_f32 v[112:113], v[28:29], v[2:3] op_sel_hi:[0,1]
	v_pk_mul_f32 v[114:115], v[28:29], v[4:5] op_sel_hi:[0,1]
	v_exp_f32_e32 v112, v112
	v_exp_f32_e32 v113, v113
	v_exp_f32_e32 v114, v114
	v_exp_f32_e32 v115, v115
	v_pk_mul_f32 v[116:117], v[88:89], v[124:125] op_sel_hi:[0,1]
	v_pk_mul_f32 v[88:89], v[88:89], v[126:127] op_sel_hi:[0,1]
	v_pk_fma_f32 v[124:125], v[108:109], v[112:113], v[116:117]
	v_pk_fma_f32 v[88:89], v[110:111], v[114:115], v[88:89]
	s_nop 0
	s_waitcnt lgkmcnt(0)
	s_nop 0
	ds_read_b128 v[108:111], v160 offset:42480
	ds_read_b128 v[112:115], v160 offset:42496
	ds_read_b128 v[116:119], v160 offset:42512
	ds_read_b128 v[120:123], v160 offset:42528
	v_pk_mul_f32 v[140:141], v[30:31], v[14:15] op_sel_hi:[0,1]
	v_exp_f32_e32 v140, v140
	v_exp_f32_e32 v141, v141
	v_pk_mul_f32 v[142:143], v[30:31], v[16:17] op_sel_hi:[0,1]
	v_exp_f32_e32 v142, v142
	v_exp_f32_e32 v143, v143
	v_mul_f32_e32 v126, v30, v25
	v_pk_mul_f32 v[90:91], v[126:127], v[90:91] op_sel_hi:[0,1]
	v_pk_fma_f32 v[128:129], v[128:129], v[140:141], v[90:91]
	v_pk_mul_f32 v[90:91], v[126:127], v[92:93] op_sel_hi:[0,1]
	v_pk_fma_f32 v[130:131], v[130:131], v[142:143], v[90:91]
	v_pk_mul_f32 v[90:91], v[30:31], v[10:11] op_sel_hi:[0,1]
	v_exp_f32_e32 v90, v90
	v_exp_f32_e32 v91, v91
	v_pk_mul_f32 v[92:93], v[30:31], v[12:13] op_sel_hi:[0,1]
	v_exp_f32_e32 v92, v92
	v_exp_f32_e32 v93, v93
	v_pk_mul_f32 v[94:95], v[126:127], v[94:95] op_sel_hi:[0,1]
	v_pk_fma_f32 v[132:133], v[132:133], v[90:91], v[94:95]
	v_pk_mul_f32 v[90:91], v[126:127], v[96:97] op_sel_hi:[0,1]
	v_pk_fma_f32 v[134:135], v[134:135], v[92:93], v[90:91]
	v_pk_mul_f32 v[90:91], v[30:31], v[6:7] op_sel_hi:[0,1]
	v_exp_f32_e32 v90, v90
	v_exp_f32_e32 v91, v91
	v_pk_mul_f32 v[92:93], v[30:31], v[8:9] op_sel_hi:[0,1]
	v_exp_f32_e32 v92, v92
	v_exp_f32_e32 v93, v93
	v_pk_mul_f32 v[94:95], v[126:127], v[98:99] op_sel_hi:[0,1]
	v_pk_fma_f32 v[136:137], v[136:137], v[90:91], v[94:95]
	v_pk_mul_f32 v[90:91], v[126:127], v[100:101] op_sel_hi:[0,1]
	v_pk_fma_f32 v[138:139], v[138:139], v[92:93], v[90:91]
	v_pk_mul_f32 v[90:91], v[30:31], v[2:3] op_sel_hi:[0,1]
	v_exp_f32_e32 v90, v90
	v_exp_f32_e32 v91, v91
	v_pk_mul_f32 v[92:93], v[30:31], v[4:5] op_sel_hi:[0,1]
	v_exp_f32_e32 v92, v92
	v_exp_f32_e32 v93, v93
	v_pk_mul_f32 v[94:95], v[126:127], v[102:103] op_sel_hi:[0,1]
	v_pk_fma_f32 v[124:125], v[124:125], v[90:91], v[94:95]
	v_pk_mul_f32 v[90:91], v[126:127], v[104:105] op_sel_hi:[0,1]
	v_pk_fma_f32 v[104:105], v[88:89], v[92:93], v[90:91]
	s_nop 0
	s_waitcnt lgkmcnt(0)
	s_nop 0
	ds_read_b128 v[88:91], v160 offset:42688
	ds_read_b128 v[92:95], v160 offset:42704
	ds_read_b128 v[96:99], v160 offset:42720
	ds_read_b128 v[100:103], v160 offset:42736
	v_pk_mul_f32 v[140:141], v[32:33], v[14:15] op_sel_hi:[0,1]
	v_exp_f32_e32 v140, v140
	v_exp_f32_e32 v141, v141
	v_pk_mul_f32 v[142:143], v[32:33], v[16:17] op_sel_hi:[0,1]
	v_exp_f32_e32 v142, v142
	v_exp_f32_e32 v143, v143
	v_mul_f32_e32 v126, v32, v87
	v_pk_mul_f32 v[108:109], v[126:127], v[108:109] op_sel_hi:[0,1]
	v_pk_fma_f32 v[128:129], v[128:129], v[140:141], v[108:109]
	v_pk_mul_f32 v[108:109], v[126:127], v[110:111] op_sel_hi:[0,1]
	v_pk_fma_f32 v[130:131], v[130:131], v[142:143], v[108:109]
	v_pk_mul_f32 v[108:109], v[32:33], v[10:11] op_sel_hi:[0,1]
	v_exp_f32_e32 v108, v108
	v_exp_f32_e32 v109, v109
	v_pk_mul_f32 v[110:111], v[32:33], v[12:13] op_sel_hi:[0,1]
	v_exp_f32_e32 v110, v110
	v_exp_f32_e32 v111, v111
	v_pk_mul_f32 v[112:113], v[126:127], v[112:113] op_sel_hi:[0,1]
	v_pk_fma_f32 v[132:133], v[132:133], v[108:109], v[112:113]
	v_pk_mul_f32 v[108:109], v[126:127], v[114:115] op_sel_hi:[0,1]
	v_pk_fma_f32 v[134:135], v[134:135], v[110:111], v[108:109]
	v_pk_mul_f32 v[108:109], v[32:33], v[6:7] op_sel_hi:[0,1]
	v_exp_f32_e32 v108, v108
	v_exp_f32_e32 v109, v109
	v_pk_mul_f32 v[110:111], v[32:33], v[8:9] op_sel_hi:[0,1]
	v_exp_f32_e32 v110, v110
	v_exp_f32_e32 v111, v111
	v_pk_mul_f32 v[112:113], v[126:127], v[116:117] op_sel_hi:[0,1]
	v_pk_fma_f32 v[136:137], v[136:137], v[108:109], v[112:113]
	v_pk_mul_f32 v[108:109], v[126:127], v[118:119] op_sel_hi:[0,1]
	v_pk_fma_f32 v[138:139], v[138:139], v[110:111], v[108:109]
	v_pk_mul_f32 v[108:109], v[32:33], v[2:3] op_sel_hi:[0,1]
	v_exp_f32_e32 v108, v108
	v_exp_f32_e32 v109, v109
	v_pk_mul_f32 v[110:111], v[32:33], v[4:5] op_sel_hi:[0,1]
	v_exp_f32_e32 v110, v110
	v_exp_f32_e32 v111, v111
	v_pk_mul_f32 v[112:113], v[126:127], v[120:121] op_sel_hi:[0,1]
	v_pk_fma_f32 v[124:125], v[124:125], v[108:109], v[112:113]
	v_pk_mul_f32 v[108:109], v[126:127], v[122:123] op_sel_hi:[0,1]
	v_pk_fma_f32 v[104:105], v[104:105], v[110:111], v[108:109]
	s_nop 0
	s_waitcnt lgkmcnt(0)
	s_nop 0
	ds_read_b128 v[108:111], v160 offset:42896
	ds_read_b128 v[112:115], v160 offset:42912
	ds_read_b128 v[116:119], v160 offset:42928
	ds_read_b128 v[120:123], v160 offset:42944
	v_pk_mul_f32 v[126:127], v[34:35], v[14:15] op_sel_hi:[0,1]
	v_exp_f32_e32 v126, v126
	v_exp_f32_e32 v127, v127
	v_pk_mul_f32 v[140:141], v[34:35], v[16:17] op_sel_hi:[0,1]
	v_exp_f32_e32 v140, v140
	v_exp_f32_e32 v141, v141
	v_mul_f32_e32 v86, v34, v86
	v_pk_mul_f32 v[88:89], v[86:87], v[88:89] op_sel_hi:[0,1]
	v_pk_fma_f32 v[126:127], v[128:129], v[126:127], v[88:89]
	v_pk_mul_f32 v[88:89], v[86:87], v[90:91] op_sel_hi:[0,1]
	v_pk_fma_f32 v[128:129], v[130:131], v[140:141], v[88:89]
	v_pk_mul_f32 v[88:89], v[34:35], v[10:11] op_sel_hi:[0,1]
	v_exp_f32_e32 v88, v88
	v_exp_f32_e32 v89, v89
	v_pk_mul_f32 v[90:91], v[34:35], v[12:13] op_sel_hi:[0,1]
	v_exp_f32_e32 v90, v90
	v_exp_f32_e32 v91, v91
	v_pk_mul_f32 v[92:93], v[86:87], v[92:93] op_sel_hi:[0,1]
	v_pk_fma_f32 v[130:131], v[132:133], v[88:89], v[92:93]
	v_pk_mul_f32 v[88:89], v[86:87], v[94:95] op_sel_hi:[0,1]
	v_pk_fma_f32 v[132:133], v[134:135], v[90:91], v[88:89]
	v_pk_mul_f32 v[88:89], v[34:35], v[6:7] op_sel_hi:[0,1]
	v_exp_f32_e32 v88, v88
	v_exp_f32_e32 v89, v89
	v_pk_mul_f32 v[90:91], v[34:35], v[8:9] op_sel_hi:[0,1]
	v_exp_f32_e32 v90, v90
	v_exp_f32_e32 v91, v91
	v_pk_mul_f32 v[92:93], v[86:87], v[96:97] op_sel_hi:[0,1]
	v_pk_fma_f32 v[134:135], v[136:137], v[88:89], v[92:93]
	v_pk_mul_f32 v[88:89], v[86:87], v[98:99] op_sel_hi:[0,1]
	v_pk_fma_f32 v[136:137], v[138:139], v[90:91], v[88:89]
	v_pk_mul_f32 v[88:89], v[34:35], v[2:3] op_sel_hi:[0,1]
	v_pk_mul_f32 v[90:91], v[34:35], v[4:5] op_sel_hi:[0,1]
	v_exp_f32_e32 v88, v88
	v_exp_f32_e32 v89, v89
	v_exp_f32_e32 v90, v90
	v_exp_f32_e32 v91, v91
	v_pk_mul_f32 v[92:93], v[86:87], v[100:101] op_sel_hi:[0,1]
	v_pk_mul_f32 v[86:87], v[86:87], v[102:103] op_sel_hi:[0,1]
	v_pk_fma_f32 v[124:125], v[124:125], v[88:89], v[92:93]
	v_pk_fma_f32 v[102:103], v[104:105], v[90:91], v[86:87]
	s_nop 0
	s_waitcnt lgkmcnt(0)
	s_nop 0
	ds_read_b128 v[86:89], v160 offset:43104
	ds_read_b128 v[90:93], v160 offset:43120
	ds_read_b128 v[94:97], v160 offset:43136
	ds_read_b128 v[98:101], v160 offset:43152
	v_pk_mul_f32 v[138:139], v[36:37], v[14:15] op_sel_hi:[0,1]
	v_exp_f32_e32 v138, v138
	v_exp_f32_e32 v139, v139
	v_pk_mul_f32 v[140:141], v[36:37], v[16:17] op_sel_hi:[0,1]
	v_exp_f32_e32 v140, v140
	v_exp_f32_e32 v141, v141
	v_mul_f32_e32 v104, v36, v85
	v_pk_mul_f32 v[108:109], v[104:105], v[108:109] op_sel_hi:[0,1]
	v_pk_fma_f32 v[126:127], v[126:127], v[138:139], v[108:109]
	v_pk_mul_f32 v[108:109], v[104:105], v[110:111] op_sel_hi:[0,1]
	v_pk_fma_f32 v[128:129], v[128:129], v[140:141], v[108:109]
	v_pk_mul_f32 v[108:109], v[36:37], v[10:11] op_sel_hi:[0,1]
	v_exp_f32_e32 v108, v108
	v_exp_f32_e32 v109, v109
	v_pk_mul_f32 v[110:111], v[36:37], v[12:13] op_sel_hi:[0,1]
	v_exp_f32_e32 v110, v110
	v_exp_f32_e32 v111, v111
	v_pk_mul_f32 v[112:113], v[104:105], v[112:113] op_sel_hi:[0,1]
	v_pk_fma_f32 v[130:131], v[130:131], v[108:109], v[112:113]
	v_pk_mul_f32 v[108:109], v[104:105], v[114:115] op_sel_hi:[0,1]
	v_pk_fma_f32 v[132:133], v[132:133], v[110:111], v[108:109]
	v_pk_mul_f32 v[108:109], v[36:37], v[6:7] op_sel_hi:[0,1]
	v_exp_f32_e32 v108, v108
	v_exp_f32_e32 v109, v109
	v_pk_mul_f32 v[110:111], v[36:37], v[8:9] op_sel_hi:[0,1]
	v_exp_f32_e32 v110, v110
	v_exp_f32_e32 v111, v111
	v_pk_mul_f32 v[112:113], v[104:105], v[116:117] op_sel_hi:[0,1]
	v_pk_fma_f32 v[134:135], v[134:135], v[108:109], v[112:113]
	v_pk_mul_f32 v[108:109], v[104:105], v[118:119] op_sel_hi:[0,1]
	v_pk_fma_f32 v[136:137], v[136:137], v[110:111], v[108:109]
	v_pk_mul_f32 v[108:109], v[36:37], v[2:3] op_sel_hi:[0,1]
	v_pk_mul_f32 v[110:111], v[36:37], v[4:5] op_sel_hi:[0,1]
	v_exp_f32_e32 v108, v108
	v_exp_f32_e32 v109, v109
	v_exp_f32_e32 v110, v110
	v_exp_f32_e32 v111, v111
	v_pk_mul_f32 v[112:113], v[104:105], v[120:121] op_sel_hi:[0,1]
	v_pk_mul_f32 v[104:105], v[104:105], v[122:123] op_sel_hi:[0,1]
	v_pk_fma_f32 v[120:121], v[124:125], v[108:109], v[112:113]
	v_pk_fma_f32 v[122:123], v[102:103], v[110:111], v[104:105]
	s_nop 0
	s_waitcnt lgkmcnt(0)
	s_nop 0
	ds_read_b128 v[102:105], v160 offset:43312
	ds_read_b128 v[108:111], v160 offset:43328
	ds_read_b128 v[112:115], v160 offset:43344
	ds_read_b128 v[116:119], v160 offset:43360
	v_pk_mul_f32 v[124:125], v[38:39], v[14:15] op_sel_hi:[0,1]
	v_exp_f32_e32 v124, v124
	v_exp_f32_e32 v125, v125
	v_pk_mul_f32 v[138:139], v[38:39], v[16:17] op_sel_hi:[0,1]
	v_exp_f32_e32 v138, v138
	v_exp_f32_e32 v139, v139
	v_mul_f32_e32 v84, v38, v84
	v_pk_mul_f32 v[86:87], v[84:85], v[86:87] op_sel_hi:[0,1]
	v_pk_fma_f32 v[124:125], v[126:127], v[124:125], v[86:87]
	v_pk_mul_f32 v[86:87], v[84:85], v[88:89] op_sel_hi:[0,1]
	v_pk_fma_f32 v[126:127], v[128:129], v[138:139], v[86:87]
	v_pk_mul_f32 v[86:87], v[38:39], v[10:11] op_sel_hi:[0,1]
	v_exp_f32_e32 v86, v86
	v_exp_f32_e32 v87, v87
	v_pk_mul_f32 v[88:89], v[38:39], v[12:13] op_sel_hi:[0,1]
	v_exp_f32_e32 v88, v88
	v_exp_f32_e32 v89, v89
	v_pk_mul_f32 v[90:91], v[84:85], v[90:91] op_sel_hi:[0,1]
	v_pk_fma_f32 v[128:129], v[130:131], v[86:87], v[90:91]
	v_pk_mul_f32 v[86:87], v[84:85], v[92:93] op_sel_hi:[0,1]
	v_pk_fma_f32 v[130:131], v[132:133], v[88:89], v[86:87]
	v_pk_mul_f32 v[86:87], v[38:39], v[6:7] op_sel_hi:[0,1]
	v_exp_f32_e32 v86, v86
	v_exp_f32_e32 v87, v87
	v_pk_mul_f32 v[88:89], v[38:39], v[8:9] op_sel_hi:[0,1]
	v_exp_f32_e32 v88, v88
	v_exp_f32_e32 v89, v89
	v_pk_mul_f32 v[90:91], v[84:85], v[94:95] op_sel_hi:[0,1]
	v_pk_fma_f32 v[132:133], v[134:135], v[86:87], v[90:91]
	v_pk_mul_f32 v[86:87], v[84:85], v[96:97] op_sel_hi:[0,1]
	v_pk_fma_f32 v[134:135], v[136:137], v[88:89], v[86:87]
	v_pk_mul_f32 v[86:87], v[38:39], v[2:3] op_sel_hi:[0,1]
	v_pk_mul_f32 v[88:89], v[38:39], v[4:5] op_sel_hi:[0,1]
	v_exp_f32_e32 v86, v86
	v_exp_f32_e32 v87, v87
	v_exp_f32_e32 v88, v88
	v_exp_f32_e32 v89, v89
	v_pk_mul_f32 v[90:91], v[84:85], v[98:99] op_sel_hi:[0,1]
	v_pk_mul_f32 v[84:85], v[84:85], v[100:101] op_sel_hi:[0,1]
	v_pk_fma_f32 v[120:121], v[120:121], v[86:87], v[90:91]
	v_pk_fma_f32 v[100:101], v[122:123], v[88:89], v[84:85]
	s_nop 0
	s_waitcnt lgkmcnt(0)
	s_nop 0
	ds_read_b128 v[84:87], v160 offset:43520
	ds_read_b128 v[88:91], v160 offset:43536
	ds_read_b128 v[92:95], v160 offset:43552
	ds_read_b128 v[96:99], v160 offset:43568
	v_pk_mul_f32 v[136:137], v[40:41], v[14:15] op_sel_hi:[0,1]
	v_exp_f32_e32 v136, v136
	v_exp_f32_e32 v137, v137
	v_pk_mul_f32 v[138:139], v[40:41], v[16:17] op_sel_hi:[0,1]
	v_exp_f32_e32 v138, v138
	v_exp_f32_e32 v139, v139
	v_mul_f32_e32 v122, v40, v83
	v_pk_mul_f32 v[102:103], v[122:123], v[102:103] op_sel_hi:[0,1]
	v_pk_fma_f32 v[124:125], v[124:125], v[136:137], v[102:103]
	v_pk_mul_f32 v[102:103], v[122:123], v[104:105] op_sel_hi:[0,1]
	v_pk_fma_f32 v[104:105], v[126:127], v[138:139], v[102:103]
	v_pk_mul_f32 v[102:103], v[40:41], v[10:11] op_sel_hi:[0,1]
	v_exp_f32_e32 v102, v102
	v_exp_f32_e32 v103, v103
	v_pk_mul_f32 v[126:127], v[40:41], v[12:13] op_sel_hi:[0,1]
	v_exp_f32_e32 v126, v126
	v_exp_f32_e32 v127, v127
	v_pk_mul_f32 v[108:109], v[122:123], v[108:109] op_sel_hi:[0,1]
	v_pk_fma_f32 v[128:129], v[128:129], v[102:103], v[108:109]
	v_pk_mul_f32 v[102:103], v[122:123], v[110:111] op_sel_hi:[0,1]
	v_pk_fma_f32 v[126:127], v[130:131], v[126:127], v[102:103]
	v_pk_mul_f32 v[102:103], v[40:41], v[6:7] op_sel_hi:[0,1]
	v_exp_f32_e32 v102, v102
	v_exp_f32_e32 v103, v103
	v_pk_mul_f32 v[108:109], v[40:41], v[8:9] op_sel_hi:[0,1]
	v_exp_f32_e32 v108, v108
	v_exp_f32_e32 v109, v109
	v_pk_mul_f32 v[110:111], v[122:123], v[112:113] op_sel_hi:[0,1]
	v_pk_fma_f32 v[130:131], v[132:133], v[102:103], v[110:111]
	v_pk_mul_f32 v[102:103], v[122:123], v[114:115] op_sel_hi:[0,1]
	v_pk_fma_f32 v[132:133], v[134:135], v[108:109], v[102:103]
	v_pk_mul_f32 v[102:103], v[40:41], v[2:3] op_sel_hi:[0,1]
	v_exp_f32_e32 v102, v102
	v_exp_f32_e32 v103, v103
	v_pk_mul_f32 v[108:109], v[40:41], v[4:5] op_sel_hi:[0,1]
	v_exp_f32_e32 v108, v108
	v_exp_f32_e32 v109, v109
	v_pk_mul_f32 v[110:111], v[122:123], v[116:117] op_sel_hi:[0,1]
	v_pk_fma_f32 v[120:121], v[120:121], v[102:103], v[110:111]
	v_pk_mul_f32 v[102:103], v[122:123], v[118:119] op_sel_hi:[0,1]
	v_pk_fma_f32 v[122:123], v[100:101], v[108:109], v[102:103]
	s_nop 0
	s_waitcnt lgkmcnt(0)
	s_nop 0
	ds_read_b128 v[100:103], v160 offset:43728
	ds_read_b128 v[108:111], v160 offset:43744
	ds_read_b128 v[112:115], v160 offset:43760
	ds_read_b128 v[116:119], v160 offset:43776
	v_pk_mul_f32 v[134:135], v[42:43], v[14:15] op_sel_hi:[0,1]
	v_exp_f32_e32 v134, v134
	v_exp_f32_e32 v135, v135
	v_pk_mul_f32 v[136:137], v[42:43], v[16:17] op_sel_hi:[0,1]
	v_exp_f32_e32 v136, v136
	v_exp_f32_e32 v137, v137
	v_mul_f32_e32 v82, v42, v82
	v_pk_mul_f32 v[84:85], v[82:83], v[84:85] op_sel_hi:[0,1]
	v_pk_fma_f32 v[124:125], v[124:125], v[134:135], v[84:85]
	v_pk_mul_f32 v[84:85], v[82:83], v[86:87] op_sel_hi:[0,1]
	v_pk_fma_f32 v[104:105], v[104:105], v[136:137], v[84:85]
	v_pk_mul_f32 v[84:85], v[42:43], v[10:11] op_sel_hi:[0,1]
	v_exp_f32_e32 v84, v84
	v_exp_f32_e32 v85, v85
	v_pk_mul_f32 v[86:87], v[42:43], v[12:13] op_sel_hi:[0,1]
	v_exp_f32_e32 v86, v86
	v_exp_f32_e32 v87, v87
	v_pk_mul_f32 v[88:89], v[82:83], v[88:89] op_sel_hi:[0,1]
	v_pk_fma_f32 v[128:129], v[128:129], v[84:85], v[88:89]
	v_pk_mul_f32 v[84:85], v[82:83], v[90:91] op_sel_hi:[0,1]
	v_pk_fma_f32 v[126:127], v[126:127], v[86:87], v[84:85]
	v_pk_mul_f32 v[84:85], v[42:43], v[6:7] op_sel_hi:[0,1]
	v_exp_f32_e32 v84, v84
	v_exp_f32_e32 v85, v85
	v_pk_mul_f32 v[86:87], v[42:43], v[8:9] op_sel_hi:[0,1]
	v_exp_f32_e32 v86, v86
	v_exp_f32_e32 v87, v87
	v_pk_mul_f32 v[88:89], v[82:83], v[92:93] op_sel_hi:[0,1]
	v_pk_fma_f32 v[130:131], v[130:131], v[84:85], v[88:89]
	v_pk_mul_f32 v[84:85], v[82:83], v[94:95] op_sel_hi:[0,1]
	v_pk_fma_f32 v[132:133], v[132:133], v[86:87], v[84:85]
	v_pk_mul_f32 v[84:85], v[42:43], v[2:3] op_sel_hi:[0,1]
	v_pk_mul_f32 v[86:87], v[42:43], v[4:5] op_sel_hi:[0,1]
	v_exp_f32_e32 v84, v84
	v_exp_f32_e32 v85, v85
	v_exp_f32_e32 v86, v86
	v_exp_f32_e32 v87, v87
	v_pk_mul_f32 v[88:89], v[82:83], v[96:97] op_sel_hi:[0,1]
	v_pk_mul_f32 v[82:83], v[82:83], v[98:99] op_sel_hi:[0,1]
	v_pk_fma_f32 v[120:121], v[120:121], v[84:85], v[88:89]
	v_pk_fma_f32 v[98:99], v[122:123], v[86:87], v[82:83]
	s_nop 0
	s_waitcnt lgkmcnt(0)
	s_nop 0
	ds_read_b128 v[82:85], v160 offset:43936
	ds_read_b128 v[86:89], v160 offset:43952
	ds_read_b128 v[90:93], v160 offset:43968
	ds_read_b128 v[94:97], v160 offset:43984
	v_pk_mul_f32 v[134:135], v[44:45], v[14:15] op_sel_hi:[0,1]
	v_exp_f32_e32 v134, v134
	v_exp_f32_e32 v135, v135
	v_pk_mul_f32 v[136:137], v[44:45], v[16:17] op_sel_hi:[0,1]
	v_exp_f32_e32 v136, v136
	v_exp_f32_e32 v137, v137
	v_mul_f32_e32 v122, v44, v81
	v_pk_mul_f32 v[100:101], v[122:123], v[100:101] op_sel_hi:[0,1]
	v_pk_fma_f32 v[124:125], v[124:125], v[134:135], v[100:101]
	v_pk_mul_f32 v[100:101], v[122:123], v[102:103] op_sel_hi:[0,1]
	v_pk_fma_f32 v[134:135], v[104:105], v[136:137], v[100:101]
	v_pk_mul_f32 v[100:101], v[44:45], v[10:11] op_sel_hi:[0,1]
	v_exp_f32_e32 v100, v100
	v_exp_f32_e32 v101, v101
	v_pk_mul_f32 v[102:103], v[44:45], v[12:13] op_sel_hi:[0,1]
	v_exp_f32_e32 v102, v102
	v_exp_f32_e32 v103, v103
	v_pk_mul_f32 v[104:105], v[122:123], v[108:109] op_sel_hi:[0,1]
	v_pk_fma_f32 v[128:129], v[128:129], v[100:101], v[104:105]
	v_pk_mul_f32 v[100:101], v[122:123], v[110:111] op_sel_hi:[0,1]
	v_pk_fma_f32 v[126:127], v[126:127], v[102:103], v[100:101]
	v_pk_mul_f32 v[100:101], v[44:45], v[6:7] op_sel_hi:[0,1]
	v_exp_f32_e32 v100, v100
	v_exp_f32_e32 v101, v101
	v_pk_mul_f32 v[102:103], v[44:45], v[8:9] op_sel_hi:[0,1]
	v_exp_f32_e32 v102, v102
	v_exp_f32_e32 v103, v103
	v_pk_mul_f32 v[104:105], v[122:123], v[112:113] op_sel_hi:[0,1]
	v_pk_fma_f32 v[130:131], v[130:131], v[100:101], v[104:105]
	v_pk_mul_f32 v[100:101], v[122:123], v[114:115] op_sel_hi:[0,1]
	v_pk_fma_f32 v[132:133], v[132:133], v[102:103], v[100:101]
	v_pk_mul_f32 v[100:101], v[44:45], v[2:3] op_sel_hi:[0,1]
	v_exp_f32_e32 v100, v100
	v_exp_f32_e32 v101, v101
	v_pk_mul_f32 v[102:103], v[44:45], v[4:5] op_sel_hi:[0,1]
	v_exp_f32_e32 v102, v102
	v_exp_f32_e32 v103, v103
	v_pk_mul_f32 v[104:105], v[122:123], v[116:117] op_sel_hi:[0,1]
	v_pk_fma_f32 v[116:117], v[120:121], v[100:101], v[104:105]
	v_pk_mul_f32 v[100:101], v[122:123], v[118:119] op_sel_hi:[0,1]
	v_pk_fma_f32 v[118:119], v[98:99], v[102:103], v[100:101]
	s_nop 0
	s_waitcnt lgkmcnt(0)
	s_nop 0
	ds_read_b128 v[98:101], v160 offset:44144
	ds_read_b128 v[102:105], v160 offset:44160
	ds_read_b128 v[108:111], v160 offset:44176
	ds_read_b128 v[112:115], v160 offset:44192
	v_pk_mul_f32 v[122:123], v[46:47], v[14:15] op_sel_hi:[0,1]
	v_exp_f32_e32 v122, v122
	v_exp_f32_e32 v123, v123
	v_pk_mul_f32 v[136:137], v[46:47], v[16:17] op_sel_hi:[0,1]
	v_exp_f32_e32 v136, v136
	v_exp_f32_e32 v137, v137
	v_mul_f32_e32 v120, v46, v79
	v_pk_mul_f32 v[82:83], v[120:121], v[82:83] op_sel_hi:[0,1]
	v_pk_fma_f32 v[122:123], v[124:125], v[122:123], v[82:83]
	v_pk_mul_f32 v[82:83], v[120:121], v[84:85] op_sel_hi:[0,1]
	v_pk_fma_f32 v[124:125], v[134:135], v[136:137], v[82:83]
	v_pk_mul_f32 v[82:83], v[46:47], v[10:11] op_sel_hi:[0,1]
	v_exp_f32_e32 v82, v82
	v_exp_f32_e32 v83, v83
	v_pk_mul_f32 v[84:85], v[46:47], v[12:13] op_sel_hi:[0,1]
	v_exp_f32_e32 v84, v84
	v_exp_f32_e32 v85, v85
	v_pk_mul_f32 v[86:87], v[120:121], v[86:87] op_sel_hi:[0,1]
	v_pk_fma_f32 v[128:129], v[128:129], v[82:83], v[86:87]
	v_pk_mul_f32 v[82:83], v[120:121], v[88:89] op_sel_hi:[0,1]
	v_pk_fma_f32 v[126:127], v[126:127], v[84:85], v[82:83]
	v_pk_mul_f32 v[82:83], v[46:47], v[6:7] op_sel_hi:[0,1]
	v_exp_f32_e32 v82, v82
	v_exp_f32_e32 v83, v83
	v_pk_mul_f32 v[84:85], v[46:47], v[8:9] op_sel_hi:[0,1]
	v_exp_f32_e32 v84, v84
	v_exp_f32_e32 v85, v85
	v_pk_mul_f32 v[86:87], v[120:121], v[90:91] op_sel_hi:[0,1]
	v_pk_fma_f32 v[130:131], v[130:131], v[82:83], v[86:87]
	v_pk_mul_f32 v[82:83], v[120:121], v[92:93] op_sel_hi:[0,1]
	v_pk_fma_f32 v[132:133], v[132:133], v[84:85], v[82:83]
	v_pk_mul_f32 v[82:83], v[46:47], v[2:3] op_sel_hi:[0,1]
	v_exp_f32_e32 v82, v82
	v_exp_f32_e32 v83, v83
	v_pk_mul_f32 v[84:85], v[46:47], v[4:5] op_sel_hi:[0,1]
	v_exp_f32_e32 v84, v84
	v_exp_f32_e32 v85, v85
	v_pk_mul_f32 v[86:87], v[120:121], v[94:95] op_sel_hi:[0,1]
	v_pk_fma_f32 v[116:117], v[116:117], v[82:83], v[86:87]
	v_pk_mul_f32 v[82:83], v[120:121], v[96:97] op_sel_hi:[0,1]
	v_pk_fma_f32 v[118:119], v[118:119], v[84:85], v[82:83]
	s_nop 0
	s_waitcnt lgkmcnt(0)
	s_nop 0
	ds_read_b128 v[82:85], v160 offset:44352
	ds_read_b128 v[86:89], v160 offset:44368
	ds_read_b128 v[90:93], v160 offset:44384
	ds_read_b128 v[94:97], v160 offset:44400
	v_pk_mul_f32 v[134:135], v[48:49], v[14:15] op_sel_hi:[0,1]
	v_exp_f32_e32 v134, v134
	v_exp_f32_e32 v135, v135
	v_pk_mul_f32 v[136:137], v[48:49], v[16:17] op_sel_hi:[0,1]
	v_exp_f32_e32 v136, v136
	v_exp_f32_e32 v137, v137
	v_mul_f32_e32 v120, v48, v77
	v_pk_mul_f32 v[98:99], v[120:121], v[98:99] op_sel_hi:[0,1]
	v_pk_fma_f32 v[122:123], v[122:123], v[134:135], v[98:99]
	v_pk_mul_f32 v[98:99], v[120:121], v[100:101] op_sel_hi:[0,1]
	v_pk_fma_f32 v[124:125], v[124:125], v[136:137], v[98:99]
	v_pk_mul_f32 v[98:99], v[48:49], v[10:11] op_sel_hi:[0,1]
	v_exp_f32_e32 v98, v98
	v_exp_f32_e32 v99, v99
	v_pk_mul_f32 v[100:101], v[48:49], v[12:13] op_sel_hi:[0,1]
	v_exp_f32_e32 v100, v100
	v_exp_f32_e32 v101, v101
	v_pk_mul_f32 v[102:103], v[120:121], v[102:103] op_sel_hi:[0,1]
	v_pk_fma_f32 v[128:129], v[128:129], v[98:99], v[102:103]
	v_pk_mul_f32 v[98:99], v[120:121], v[104:105] op_sel_hi:[0,1]
	v_pk_fma_f32 v[126:127], v[126:127], v[100:101], v[98:99]
	v_pk_mul_f32 v[98:99], v[48:49], v[6:7] op_sel_hi:[0,1]
	v_exp_f32_e32 v98, v98
	v_exp_f32_e32 v99, v99
	v_pk_mul_f32 v[100:101], v[48:49], v[8:9] op_sel_hi:[0,1]
	v_exp_f32_e32 v100, v100
	v_exp_f32_e32 v101, v101
	v_pk_mul_f32 v[102:103], v[120:121], v[108:109] op_sel_hi:[0,1]
	v_pk_fma_f32 v[130:131], v[130:131], v[98:99], v[102:103]
	v_pk_mul_f32 v[98:99], v[120:121], v[110:111] op_sel_hi:[0,1]
	v_pk_fma_f32 v[132:133], v[132:133], v[100:101], v[98:99]
	v_pk_mul_f32 v[98:99], v[48:49], v[2:3] op_sel_hi:[0,1]
	v_exp_f32_e32 v98, v98
	v_exp_f32_e32 v99, v99
	v_pk_mul_f32 v[100:101], v[48:49], v[4:5] op_sel_hi:[0,1]
	v_exp_f32_e32 v100, v100
	v_exp_f32_e32 v101, v101
	v_pk_mul_f32 v[102:103], v[120:121], v[112:113] op_sel_hi:[0,1]
	v_pk_fma_f32 v[116:117], v[116:117], v[98:99], v[102:103]
	v_pk_mul_f32 v[98:99], v[120:121], v[114:115] op_sel_hi:[0,1]
	v_pk_fma_f32 v[118:119], v[118:119], v[100:101], v[98:99]
	s_nop 0
	s_waitcnt lgkmcnt(0)
	s_nop 0
	ds_read_b128 v[98:101], v160 offset:44560
	ds_read_b128 v[102:105], v160 offset:44576
	ds_read_b128 v[108:111], v160 offset:44592
	ds_read_b128 v[112:115], v160 offset:44608
	v_pk_mul_f32 v[134:135], v[50:51], v[14:15] op_sel_hi:[0,1]
	v_exp_f32_e32 v134, v134
	v_exp_f32_e32 v135, v135
	v_pk_mul_f32 v[136:137], v[50:51], v[16:17] op_sel_hi:[0,1]
	v_exp_f32_e32 v136, v136
	v_exp_f32_e32 v137, v137
	v_mul_f32_e32 v120, v50, v75
	v_pk_mul_f32 v[82:83], v[120:121], v[82:83] op_sel_hi:[0,1]
	v_pk_fma_f32 v[122:123], v[122:123], v[134:135], v[82:83]
	v_pk_mul_f32 v[82:83], v[120:121], v[84:85] op_sel_hi:[0,1]
	v_pk_fma_f32 v[124:125], v[124:125], v[136:137], v[82:83]
	v_pk_mul_f32 v[82:83], v[50:51], v[10:11] op_sel_hi:[0,1]
	v_exp_f32_e32 v82, v82
	v_exp_f32_e32 v83, v83
	v_pk_mul_f32 v[84:85], v[50:51], v[12:13] op_sel_hi:[0,1]
	v_exp_f32_e32 v84, v84
	v_exp_f32_e32 v85, v85
	v_pk_mul_f32 v[86:87], v[120:121], v[86:87] op_sel_hi:[0,1]
	v_pk_fma_f32 v[128:129], v[128:129], v[82:83], v[86:87]
	v_pk_mul_f32 v[82:83], v[120:121], v[88:89] op_sel_hi:[0,1]
	v_pk_fma_f32 v[126:127], v[126:127], v[84:85], v[82:83]
	v_pk_mul_f32 v[82:83], v[50:51], v[6:7] op_sel_hi:[0,1]
	v_exp_f32_e32 v82, v82
	v_exp_f32_e32 v83, v83
	v_pk_mul_f32 v[84:85], v[50:51], v[8:9] op_sel_hi:[0,1]
	v_exp_f32_e32 v84, v84
	v_exp_f32_e32 v85, v85
	v_pk_mul_f32 v[86:87], v[120:121], v[90:91] op_sel_hi:[0,1]
	v_pk_fma_f32 v[130:131], v[130:131], v[82:83], v[86:87]
	v_pk_mul_f32 v[82:83], v[120:121], v[92:93] op_sel_hi:[0,1]
	v_pk_fma_f32 v[132:133], v[132:133], v[84:85], v[82:83]
	v_pk_mul_f32 v[82:83], v[50:51], v[2:3] op_sel_hi:[0,1]
	v_exp_f32_e32 v82, v82
	v_exp_f32_e32 v83, v83
	v_pk_mul_f32 v[84:85], v[50:51], v[4:5] op_sel_hi:[0,1]
	v_exp_f32_e32 v84, v84
	v_exp_f32_e32 v85, v85
	v_pk_mul_f32 v[86:87], v[120:121], v[94:95] op_sel_hi:[0,1]
	v_pk_fma_f32 v[116:117], v[116:117], v[82:83], v[86:87]
	v_pk_mul_f32 v[82:83], v[120:121], v[96:97] op_sel_hi:[0,1]
	v_pk_fma_f32 v[118:119], v[118:119], v[84:85], v[82:83]
	s_nop 0
	s_waitcnt lgkmcnt(0)
	s_nop 0
	ds_read_b128 v[82:85], v160 offset:44768
	ds_read_b128 v[86:89], v160 offset:44784
	ds_read_b128 v[90:93], v160 offset:44800
	ds_read_b128 v[94:97], v160 offset:44816
	v_pk_mul_f32 v[134:135], v[52:53], v[14:15] op_sel_hi:[0,1]
	v_exp_f32_e32 v134, v134
	v_exp_f32_e32 v135, v135
	v_pk_mul_f32 v[136:137], v[52:53], v[16:17] op_sel_hi:[0,1]
	v_exp_f32_e32 v136, v136
	v_exp_f32_e32 v137, v137
	v_mul_f32_e32 v120, v52, v73
	v_pk_mul_f32 v[98:99], v[120:121], v[98:99] op_sel_hi:[0,1]
	v_pk_fma_f32 v[122:123], v[122:123], v[134:135], v[98:99]
	v_pk_mul_f32 v[98:99], v[120:121], v[100:101] op_sel_hi:[0,1]
	v_pk_fma_f32 v[124:125], v[124:125], v[136:137], v[98:99]
	v_pk_mul_f32 v[98:99], v[52:53], v[10:11] op_sel_hi:[0,1]
	v_exp_f32_e32 v98, v98
	v_exp_f32_e32 v99, v99
	v_pk_mul_f32 v[100:101], v[52:53], v[12:13] op_sel_hi:[0,1]
	v_exp_f32_e32 v100, v100
	v_exp_f32_e32 v101, v101
	v_pk_mul_f32 v[102:103], v[120:121], v[102:103] op_sel_hi:[0,1]
	v_pk_fma_f32 v[128:129], v[128:129], v[98:99], v[102:103]
	v_pk_mul_f32 v[98:99], v[120:121], v[104:105] op_sel_hi:[0,1]
	v_pk_fma_f32 v[126:127], v[126:127], v[100:101], v[98:99]
	v_pk_mul_f32 v[98:99], v[52:53], v[6:7] op_sel_hi:[0,1]
	v_exp_f32_e32 v98, v98
	v_exp_f32_e32 v99, v99
	v_pk_mul_f32 v[100:101], v[52:53], v[8:9] op_sel_hi:[0,1]
	v_exp_f32_e32 v100, v100
	v_exp_f32_e32 v101, v101
	v_pk_mul_f32 v[102:103], v[120:121], v[108:109] op_sel_hi:[0,1]
	v_pk_fma_f32 v[130:131], v[130:131], v[98:99], v[102:103]
	v_pk_mul_f32 v[98:99], v[120:121], v[110:111] op_sel_hi:[0,1]
	v_pk_fma_f32 v[132:133], v[132:133], v[100:101], v[98:99]
	v_pk_mul_f32 v[98:99], v[52:53], v[2:3] op_sel_hi:[0,1]
	v_exp_f32_e32 v98, v98
	v_exp_f32_e32 v99, v99
	v_pk_mul_f32 v[100:101], v[52:53], v[4:5] op_sel_hi:[0,1]
	v_exp_f32_e32 v100, v100
	v_exp_f32_e32 v101, v101
	v_pk_mul_f32 v[102:103], v[120:121], v[112:113] op_sel_hi:[0,1]
	v_pk_fma_f32 v[116:117], v[116:117], v[98:99], v[102:103]
	v_pk_mul_f32 v[98:99], v[120:121], v[114:115] op_sel_hi:[0,1]
	v_pk_fma_f32 v[118:119], v[118:119], v[100:101], v[98:99]
	s_nop 0
	s_waitcnt lgkmcnt(0)
	s_nop 0
	ds_read_b128 v[98:101], v160 offset:44976
	ds_read_b128 v[102:105], v160 offset:44992
	ds_read_b128 v[108:111], v160 offset:45008
	ds_read_b128 v[112:115], v160 offset:45024
	v_pk_mul_f32 v[134:135], v[54:55], v[14:15] op_sel_hi:[0,1]
	v_exp_f32_e32 v134, v134
	v_exp_f32_e32 v135, v135
	v_pk_mul_f32 v[136:137], v[54:55], v[16:17] op_sel_hi:[0,1]
	v_exp_f32_e32 v136, v136
	v_exp_f32_e32 v137, v137
	v_mul_f32_e32 v120, v54, v71
	v_pk_mul_f32 v[82:83], v[120:121], v[82:83] op_sel_hi:[0,1]
	v_pk_fma_f32 v[122:123], v[122:123], v[134:135], v[82:83]
	v_pk_mul_f32 v[82:83], v[120:121], v[84:85] op_sel_hi:[0,1]
	v_pk_fma_f32 v[124:125], v[124:125], v[136:137], v[82:83]
	v_pk_mul_f32 v[82:83], v[54:55], v[10:11] op_sel_hi:[0,1]
	v_exp_f32_e32 v82, v82
	v_exp_f32_e32 v83, v83
	v_pk_mul_f32 v[84:85], v[54:55], v[12:13] op_sel_hi:[0,1]
	v_exp_f32_e32 v84, v84
	v_exp_f32_e32 v85, v85
	v_pk_mul_f32 v[86:87], v[120:121], v[86:87] op_sel_hi:[0,1]
	v_pk_fma_f32 v[128:129], v[128:129], v[82:83], v[86:87]
	v_pk_mul_f32 v[82:83], v[120:121], v[88:89] op_sel_hi:[0,1]
	v_pk_fma_f32 v[126:127], v[126:127], v[84:85], v[82:83]
	v_pk_mul_f32 v[82:83], v[54:55], v[6:7] op_sel_hi:[0,1]
	v_exp_f32_e32 v82, v82
	v_exp_f32_e32 v83, v83
	v_pk_mul_f32 v[84:85], v[54:55], v[8:9] op_sel_hi:[0,1]
	v_exp_f32_e32 v84, v84
	v_exp_f32_e32 v85, v85
	v_pk_mul_f32 v[86:87], v[120:121], v[90:91] op_sel_hi:[0,1]
	v_pk_fma_f32 v[130:131], v[130:131], v[82:83], v[86:87]
	v_pk_mul_f32 v[82:83], v[120:121], v[92:93] op_sel_hi:[0,1]
	v_pk_fma_f32 v[132:133], v[132:133], v[84:85], v[82:83]
	v_pk_mul_f32 v[82:83], v[54:55], v[2:3] op_sel_hi:[0,1]
	v_exp_f32_e32 v82, v82
	v_exp_f32_e32 v83, v83
	v_pk_mul_f32 v[84:85], v[54:55], v[4:5] op_sel_hi:[0,1]
	v_exp_f32_e32 v84, v84
	v_exp_f32_e32 v85, v85
	v_pk_mul_f32 v[86:87], v[120:121], v[94:95] op_sel_hi:[0,1]
	v_pk_fma_f32 v[116:117], v[116:117], v[82:83], v[86:87]
	v_pk_mul_f32 v[82:83], v[120:121], v[96:97] op_sel_hi:[0,1]
	v_pk_fma_f32 v[118:119], v[118:119], v[84:85], v[82:83]
	s_nop 0
	s_waitcnt lgkmcnt(0)
	s_nop 0
	ds_read_b128 v[82:85], v160 offset:45184
	ds_read_b128 v[86:89], v160 offset:45200
	ds_read_b128 v[90:93], v160 offset:45216
	ds_read_b128 v[94:97], v160 offset:45232
	v_pk_mul_f32 v[134:135], v[56:57], v[14:15] op_sel_hi:[0,1]
	v_exp_f32_e32 v134, v134
	v_exp_f32_e32 v135, v135
	v_pk_mul_f32 v[136:137], v[56:57], v[16:17] op_sel_hi:[0,1]
	v_exp_f32_e32 v136, v136
	v_exp_f32_e32 v137, v137
	v_mul_f32_e32 v120, v56, v69
	v_pk_mul_f32 v[98:99], v[120:121], v[98:99] op_sel_hi:[0,1]
	v_pk_fma_f32 v[122:123], v[122:123], v[134:135], v[98:99]
	v_pk_mul_f32 v[98:99], v[120:121], v[100:101] op_sel_hi:[0,1]
	v_pk_fma_f32 v[124:125], v[124:125], v[136:137], v[98:99]
	v_pk_mul_f32 v[98:99], v[56:57], v[10:11] op_sel_hi:[0,1]
	v_exp_f32_e32 v98, v98
	v_exp_f32_e32 v99, v99
	v_pk_mul_f32 v[100:101], v[56:57], v[12:13] op_sel_hi:[0,1]
	v_exp_f32_e32 v100, v100
	v_exp_f32_e32 v101, v101
	v_pk_mul_f32 v[102:103], v[120:121], v[102:103] op_sel_hi:[0,1]
	v_pk_fma_f32 v[128:129], v[128:129], v[98:99], v[102:103]
	v_pk_mul_f32 v[98:99], v[120:121], v[104:105] op_sel_hi:[0,1]
	v_pk_fma_f32 v[126:127], v[126:127], v[100:101], v[98:99]
	v_pk_mul_f32 v[98:99], v[56:57], v[6:7] op_sel_hi:[0,1]
	v_exp_f32_e32 v98, v98
	v_exp_f32_e32 v99, v99
	v_pk_mul_f32 v[100:101], v[56:57], v[8:9] op_sel_hi:[0,1]
	v_exp_f32_e32 v100, v100
	v_exp_f32_e32 v101, v101
	v_pk_mul_f32 v[102:103], v[120:121], v[108:109] op_sel_hi:[0,1]
	v_pk_fma_f32 v[130:131], v[130:131], v[98:99], v[102:103]
	v_pk_mul_f32 v[98:99], v[120:121], v[110:111] op_sel_hi:[0,1]
	v_pk_fma_f32 v[132:133], v[132:133], v[100:101], v[98:99]
	v_pk_mul_f32 v[98:99], v[56:57], v[2:3] op_sel_hi:[0,1]
	v_exp_f32_e32 v98, v98
	v_exp_f32_e32 v99, v99
	v_pk_mul_f32 v[100:101], v[56:57], v[4:5] op_sel_hi:[0,1]
	v_exp_f32_e32 v100, v100
	v_exp_f32_e32 v101, v101
	v_pk_mul_f32 v[102:103], v[120:121], v[112:113] op_sel_hi:[0,1]
	v_pk_fma_f32 v[116:117], v[116:117], v[98:99], v[102:103]
	v_pk_mul_f32 v[98:99], v[120:121], v[114:115] op_sel_hi:[0,1]
	v_pk_fma_f32 v[118:119], v[118:119], v[100:101], v[98:99]
	s_nop 0
	s_waitcnt lgkmcnt(0)
	s_nop 0
	ds_read_b128 v[98:101], v160 offset:45392
	ds_read_b128 v[102:105], v160 offset:45408
	ds_read_b128 v[108:111], v160 offset:45424
	ds_read_b128 v[112:115], v160 offset:45440
	v_pk_mul_f32 v[134:135], v[58:59], v[14:15] op_sel_hi:[0,1]
	v_exp_f32_e32 v134, v134
	v_exp_f32_e32 v135, v135
	v_pk_mul_f32 v[136:137], v[58:59], v[16:17] op_sel_hi:[0,1]
	v_exp_f32_e32 v136, v136
	v_exp_f32_e32 v137, v137
	v_mul_f32_e32 v120, v58, v67
	v_pk_mul_f32 v[82:83], v[120:121], v[82:83] op_sel_hi:[0,1]
	v_pk_fma_f32 v[122:123], v[122:123], v[134:135], v[82:83]
	v_pk_mul_f32 v[82:83], v[120:121], v[84:85] op_sel_hi:[0,1]
	v_pk_fma_f32 v[124:125], v[124:125], v[136:137], v[82:83]
	v_pk_mul_f32 v[82:83], v[58:59], v[10:11] op_sel_hi:[0,1]
	v_exp_f32_e32 v82, v82
	v_exp_f32_e32 v83, v83
	v_pk_mul_f32 v[84:85], v[58:59], v[12:13] op_sel_hi:[0,1]
	v_exp_f32_e32 v84, v84
	v_exp_f32_e32 v85, v85
	v_pk_mul_f32 v[86:87], v[120:121], v[86:87] op_sel_hi:[0,1]
	v_pk_fma_f32 v[128:129], v[128:129], v[82:83], v[86:87]
	v_pk_mul_f32 v[82:83], v[120:121], v[88:89] op_sel_hi:[0,1]
	v_pk_fma_f32 v[126:127], v[126:127], v[84:85], v[82:83]
	v_pk_mul_f32 v[82:83], v[58:59], v[6:7] op_sel_hi:[0,1]
	v_exp_f32_e32 v82, v82
	v_exp_f32_e32 v83, v83
	v_pk_mul_f32 v[84:85], v[58:59], v[8:9] op_sel_hi:[0,1]
	v_exp_f32_e32 v84, v84
	v_exp_f32_e32 v85, v85
	v_pk_mul_f32 v[86:87], v[120:121], v[90:91] op_sel_hi:[0,1]
	v_pk_fma_f32 v[130:131], v[130:131], v[82:83], v[86:87]
	v_pk_mul_f32 v[82:83], v[120:121], v[92:93] op_sel_hi:[0,1]
	v_pk_fma_f32 v[132:133], v[132:133], v[84:85], v[82:83]
	v_pk_mul_f32 v[82:83], v[58:59], v[2:3] op_sel_hi:[0,1]
	v_exp_f32_e32 v82, v82
	v_exp_f32_e32 v83, v83
	v_pk_mul_f32 v[84:85], v[58:59], v[4:5] op_sel_hi:[0,1]
	v_exp_f32_e32 v84, v84
	v_exp_f32_e32 v85, v85
	v_pk_mul_f32 v[86:87], v[120:121], v[94:95] op_sel_hi:[0,1]
	v_pk_fma_f32 v[116:117], v[116:117], v[82:83], v[86:87]
	v_pk_mul_f32 v[82:83], v[120:121], v[96:97] op_sel_hi:[0,1]
	v_pk_fma_f32 v[118:119], v[118:119], v[84:85], v[82:83]
	s_nop 0
	s_waitcnt lgkmcnt(0)
	s_nop 0
	ds_read_b128 v[82:85], v160 offset:45600
	ds_read_b128 v[86:89], v160 offset:45616
	ds_read_b128 v[90:93], v160 offset:45632
	ds_read_b128 v[94:97], v160 offset:45648
	v_pk_mul_f32 v[134:135], v[60:61], v[14:15] op_sel_hi:[0,1]
	v_exp_f32_e32 v134, v134
	v_exp_f32_e32 v135, v135
	v_pk_mul_f32 v[136:137], v[60:61], v[16:17] op_sel_hi:[0,1]
	v_exp_f32_e32 v136, v136
	v_exp_f32_e32 v137, v137
	v_mul_f32_e32 v120, v60, v65
	v_pk_mul_f32 v[98:99], v[120:121], v[98:99] op_sel_hi:[0,1]
	v_pk_fma_f32 v[122:123], v[122:123], v[134:135], v[98:99]
	v_pk_mul_f32 v[98:99], v[120:121], v[100:101] op_sel_hi:[0,1]
	v_pk_fma_f32 v[124:125], v[124:125], v[136:137], v[98:99]
	v_pk_mul_f32 v[98:99], v[60:61], v[10:11] op_sel_hi:[0,1]
	v_exp_f32_e32 v98, v98
	v_exp_f32_e32 v99, v99
	v_pk_mul_f32 v[100:101], v[60:61], v[12:13] op_sel_hi:[0,1]
	v_exp_f32_e32 v100, v100
	v_exp_f32_e32 v101, v101
	v_pk_mul_f32 v[102:103], v[120:121], v[102:103] op_sel_hi:[0,1]
	v_pk_fma_f32 v[128:129], v[128:129], v[98:99], v[102:103]
	v_pk_mul_f32 v[98:99], v[120:121], v[104:105] op_sel_hi:[0,1]
	v_pk_fma_f32 v[126:127], v[126:127], v[100:101], v[98:99]
	v_pk_mul_f32 v[98:99], v[60:61], v[6:7] op_sel_hi:[0,1]
	v_exp_f32_e32 v98, v98
	v_exp_f32_e32 v99, v99
	v_pk_mul_f32 v[100:101], v[60:61], v[8:9] op_sel_hi:[0,1]
	v_exp_f32_e32 v100, v100
	v_exp_f32_e32 v101, v101
	v_pk_mul_f32 v[102:103], v[120:121], v[108:109] op_sel_hi:[0,1]
	v_pk_fma_f32 v[130:131], v[130:131], v[98:99], v[102:103]
	v_pk_mul_f32 v[98:99], v[120:121], v[110:111] op_sel_hi:[0,1]
	v_pk_fma_f32 v[132:133], v[132:133], v[100:101], v[98:99]
	v_pk_mul_f32 v[98:99], v[60:61], v[2:3] op_sel_hi:[0,1]
	v_exp_f32_e32 v98, v98
	v_exp_f32_e32 v99, v99
	v_pk_mul_f32 v[100:101], v[60:61], v[4:5] op_sel_hi:[0,1]
	v_exp_f32_e32 v100, v100
	v_exp_f32_e32 v101, v101
	v_pk_mul_f32 v[102:103], v[120:121], v[112:113] op_sel_hi:[0,1]
	v_pk_fma_f32 v[116:117], v[116:117], v[98:99], v[102:103]
	v_pk_mul_f32 v[98:99], v[120:121], v[114:115] op_sel_hi:[0,1]
	v_pk_fma_f32 v[118:119], v[118:119], v[100:101], v[98:99]
	s_nop 0
	s_waitcnt lgkmcnt(0)
	s_nop 0
	ds_read_b128 v[98:101], v160 offset:45808
	ds_read_b128 v[102:105], v160 offset:45824
	ds_read_b128 v[108:111], v160 offset:45840
	ds_read_b128 v[112:115], v160 offset:45856
	v_pk_mul_f32 v[134:135], v[62:63], v[14:15] op_sel_hi:[0,1]
	v_exp_f32_e32 v134, v134
	v_exp_f32_e32 v135, v135
	v_pk_mul_f32 v[136:137], v[62:63], v[16:17] op_sel_hi:[0,1]
	v_exp_f32_e32 v136, v136
	v_exp_f32_e32 v137, v137
	v_mul_f32_e32 v120, v62, v63
	v_pk_mul_f32 v[82:83], v[120:121], v[82:83] op_sel_hi:[0,1]
	v_pk_fma_f32 v[122:123], v[122:123], v[134:135], v[82:83]
	v_pk_mul_f32 v[82:83], v[120:121], v[84:85] op_sel_hi:[0,1]
	v_pk_fma_f32 v[124:125], v[124:125], v[136:137], v[82:83]
	v_pk_mul_f32 v[82:83], v[62:63], v[10:11] op_sel_hi:[0,1]
	v_exp_f32_e32 v82, v82
	v_exp_f32_e32 v83, v83
	v_pk_mul_f32 v[84:85], v[62:63], v[12:13] op_sel_hi:[0,1]
	v_exp_f32_e32 v84, v84
	v_exp_f32_e32 v85, v85
	v_pk_mul_f32 v[86:87], v[120:121], v[86:87] op_sel_hi:[0,1]
	v_pk_fma_f32 v[128:129], v[128:129], v[82:83], v[86:87]
	v_pk_mul_f32 v[82:83], v[120:121], v[88:89] op_sel_hi:[0,1]
	v_pk_fma_f32 v[126:127], v[126:127], v[84:85], v[82:83]
	v_pk_mul_f32 v[82:83], v[62:63], v[6:7] op_sel_hi:[0,1]
	v_exp_f32_e32 v82, v82
	v_exp_f32_e32 v83, v83
	v_pk_mul_f32 v[84:85], v[62:63], v[8:9] op_sel_hi:[0,1]
	v_exp_f32_e32 v84, v84
	v_exp_f32_e32 v85, v85
	v_pk_mul_f32 v[86:87], v[120:121], v[90:91] op_sel_hi:[0,1]
	v_pk_fma_f32 v[130:131], v[130:131], v[82:83], v[86:87]
	v_pk_mul_f32 v[82:83], v[120:121], v[92:93] op_sel_hi:[0,1]
	v_pk_fma_f32 v[132:133], v[132:133], v[84:85], v[82:83]
	v_pk_mul_f32 v[82:83], v[62:63], v[2:3] op_sel_hi:[0,1]
	v_exp_f32_e32 v82, v82
	v_exp_f32_e32 v83, v83
	v_pk_mul_f32 v[84:85], v[62:63], v[4:5] op_sel_hi:[0,1]
	v_exp_f32_e32 v84, v84
	v_exp_f32_e32 v85, v85
	v_pk_mul_f32 v[86:87], v[120:121], v[94:95] op_sel_hi:[0,1]
	v_pk_fma_f32 v[116:117], v[116:117], v[82:83], v[86:87]
	v_pk_mul_f32 v[82:83], v[120:121], v[96:97] op_sel_hi:[0,1]
	v_pk_fma_f32 v[118:119], v[118:119], v[84:85], v[82:83]
	s_nop 0
	s_waitcnt lgkmcnt(0)
	s_nop 0
	ds_read_b128 v[82:85], v160 offset:46016
	ds_read_b128 v[86:89], v160 offset:46032
	ds_read_b128 v[90:93], v160 offset:46048
	ds_read_b128 v[94:97], v160 offset:46064
	v_pk_mul_f32 v[134:135], v[64:65], v[14:15] op_sel_hi:[0,1]
	v_exp_f32_e32 v134, v134
	v_exp_f32_e32 v135, v135
	v_pk_mul_f32 v[136:137], v[64:65], v[16:17] op_sel_hi:[0,1]
	v_exp_f32_e32 v136, v136
	v_exp_f32_e32 v137, v137
	v_mul_f32_e32 v120, v64, v61
	v_pk_mul_f32 v[98:99], v[120:121], v[98:99] op_sel_hi:[0,1]
	v_pk_fma_f32 v[122:123], v[122:123], v[134:135], v[98:99]
	v_pk_mul_f32 v[98:99], v[120:121], v[100:101] op_sel_hi:[0,1]
	v_pk_fma_f32 v[124:125], v[124:125], v[136:137], v[98:99]
	v_pk_mul_f32 v[98:99], v[64:65], v[10:11] op_sel_hi:[0,1]
	v_exp_f32_e32 v98, v98
	v_exp_f32_e32 v99, v99
	v_pk_mul_f32 v[100:101], v[64:65], v[12:13] op_sel_hi:[0,1]
	v_exp_f32_e32 v100, v100
	v_exp_f32_e32 v101, v101
	v_pk_mul_f32 v[102:103], v[120:121], v[102:103] op_sel_hi:[0,1]
	v_pk_fma_f32 v[128:129], v[128:129], v[98:99], v[102:103]
	v_pk_mul_f32 v[98:99], v[120:121], v[104:105] op_sel_hi:[0,1]
	v_pk_fma_f32 v[126:127], v[126:127], v[100:101], v[98:99]
	v_pk_mul_f32 v[98:99], v[64:65], v[6:7] op_sel_hi:[0,1]
	v_exp_f32_e32 v98, v98
	v_exp_f32_e32 v99, v99
	v_pk_mul_f32 v[100:101], v[64:65], v[8:9] op_sel_hi:[0,1]
	v_exp_f32_e32 v100, v100
	v_exp_f32_e32 v101, v101
	v_pk_mul_f32 v[102:103], v[120:121], v[108:109] op_sel_hi:[0,1]
	v_pk_fma_f32 v[130:131], v[130:131], v[98:99], v[102:103]
	v_pk_mul_f32 v[98:99], v[120:121], v[110:111] op_sel_hi:[0,1]
	v_pk_fma_f32 v[132:133], v[132:133], v[100:101], v[98:99]
	v_pk_mul_f32 v[98:99], v[64:65], v[2:3] op_sel_hi:[0,1]
	v_exp_f32_e32 v98, v98
	v_exp_f32_e32 v99, v99
	v_pk_mul_f32 v[100:101], v[64:65], v[4:5] op_sel_hi:[0,1]
	v_exp_f32_e32 v100, v100
	v_exp_f32_e32 v101, v101
	v_pk_mul_f32 v[102:103], v[120:121], v[112:113] op_sel_hi:[0,1]
	v_pk_fma_f32 v[116:117], v[116:117], v[98:99], v[102:103]
	v_pk_mul_f32 v[98:99], v[120:121], v[114:115] op_sel_hi:[0,1]
	v_pk_fma_f32 v[118:119], v[118:119], v[100:101], v[98:99]
	s_nop 0
	s_waitcnt lgkmcnt(0)
	s_nop 0
	ds_read_b128 v[98:101], v160 offset:46224
	ds_read_b128 v[102:105], v160 offset:46240
	ds_read_b128 v[108:111], v160 offset:46256
	ds_read_b128 v[112:115], v160 offset:46272
	v_pk_mul_f32 v[134:135], v[66:67], v[14:15] op_sel_hi:[0,1]
	v_exp_f32_e32 v134, v134
	v_exp_f32_e32 v135, v135
	v_pk_mul_f32 v[136:137], v[66:67], v[16:17] op_sel_hi:[0,1]
	v_exp_f32_e32 v136, v136
	v_exp_f32_e32 v137, v137
	v_mul_f32_e32 v120, v66, v59
	v_pk_mul_f32 v[82:83], v[120:121], v[82:83] op_sel_hi:[0,1]
	v_pk_fma_f32 v[122:123], v[122:123], v[134:135], v[82:83]
	v_pk_mul_f32 v[82:83], v[120:121], v[84:85] op_sel_hi:[0,1]
	v_pk_fma_f32 v[124:125], v[124:125], v[136:137], v[82:83]
	v_pk_mul_f32 v[82:83], v[66:67], v[10:11] op_sel_hi:[0,1]
	v_exp_f32_e32 v82, v82
	v_exp_f32_e32 v83, v83
	v_pk_mul_f32 v[84:85], v[66:67], v[12:13] op_sel_hi:[0,1]
	v_exp_f32_e32 v84, v84
	v_exp_f32_e32 v85, v85
	v_pk_mul_f32 v[86:87], v[120:121], v[86:87] op_sel_hi:[0,1]
	v_pk_fma_f32 v[128:129], v[128:129], v[82:83], v[86:87]
	v_pk_mul_f32 v[82:83], v[120:121], v[88:89] op_sel_hi:[0,1]
	v_pk_fma_f32 v[126:127], v[126:127], v[84:85], v[82:83]
	v_pk_mul_f32 v[82:83], v[66:67], v[6:7] op_sel_hi:[0,1]
	v_exp_f32_e32 v82, v82
	v_exp_f32_e32 v83, v83
	v_pk_mul_f32 v[84:85], v[66:67], v[8:9] op_sel_hi:[0,1]
	v_exp_f32_e32 v84, v84
	v_exp_f32_e32 v85, v85
	v_pk_mul_f32 v[86:87], v[120:121], v[90:91] op_sel_hi:[0,1]
	v_pk_fma_f32 v[130:131], v[130:131], v[82:83], v[86:87]
	v_pk_mul_f32 v[82:83], v[120:121], v[92:93] op_sel_hi:[0,1]
	v_pk_fma_f32 v[132:133], v[132:133], v[84:85], v[82:83]
	v_pk_mul_f32 v[82:83], v[66:67], v[2:3] op_sel_hi:[0,1]
	v_exp_f32_e32 v82, v82
	v_exp_f32_e32 v83, v83
	v_pk_mul_f32 v[84:85], v[66:67], v[4:5] op_sel_hi:[0,1]
	v_exp_f32_e32 v84, v84
	v_exp_f32_e32 v85, v85
	v_pk_mul_f32 v[86:87], v[120:121], v[94:95] op_sel_hi:[0,1]
	v_pk_fma_f32 v[116:117], v[116:117], v[82:83], v[86:87]
	v_pk_mul_f32 v[82:83], v[120:121], v[96:97] op_sel_hi:[0,1]
	v_pk_fma_f32 v[118:119], v[118:119], v[84:85], v[82:83]
	s_nop 0
	s_waitcnt lgkmcnt(0)
	s_nop 0
	ds_read_b128 v[82:85], v160 offset:46432
	ds_read_b128 v[86:89], v160 offset:46448
	ds_read_b128 v[90:93], v160 offset:46464
	ds_read_b128 v[94:97], v160 offset:46480
	v_pk_mul_f32 v[134:135], v[68:69], v[14:15] op_sel_hi:[0,1]
	v_exp_f32_e32 v134, v134
	v_exp_f32_e32 v135, v135
	v_pk_mul_f32 v[136:137], v[68:69], v[16:17] op_sel_hi:[0,1]
	v_exp_f32_e32 v136, v136
	v_exp_f32_e32 v137, v137
	v_mul_f32_e32 v120, v68, v57
	v_pk_mul_f32 v[98:99], v[120:121], v[98:99] op_sel_hi:[0,1]
	v_pk_fma_f32 v[122:123], v[122:123], v[134:135], v[98:99]
	v_pk_mul_f32 v[98:99], v[120:121], v[100:101] op_sel_hi:[0,1]
	v_pk_fma_f32 v[124:125], v[124:125], v[136:137], v[98:99]
	v_pk_mul_f32 v[98:99], v[68:69], v[10:11] op_sel_hi:[0,1]
	v_exp_f32_e32 v98, v98
	v_exp_f32_e32 v99, v99
	v_pk_mul_f32 v[100:101], v[68:69], v[12:13] op_sel_hi:[0,1]
	v_exp_f32_e32 v100, v100
	v_exp_f32_e32 v101, v101
	v_pk_mul_f32 v[102:103], v[120:121], v[102:103] op_sel_hi:[0,1]
	v_pk_fma_f32 v[128:129], v[128:129], v[98:99], v[102:103]
	v_pk_mul_f32 v[98:99], v[120:121], v[104:105] op_sel_hi:[0,1]
	v_pk_fma_f32 v[126:127], v[126:127], v[100:101], v[98:99]
	v_pk_mul_f32 v[98:99], v[68:69], v[6:7] op_sel_hi:[0,1]
	v_exp_f32_e32 v98, v98
	v_exp_f32_e32 v99, v99
	v_pk_mul_f32 v[100:101], v[68:69], v[8:9] op_sel_hi:[0,1]
	v_exp_f32_e32 v100, v100
	v_exp_f32_e32 v101, v101
	v_pk_mul_f32 v[102:103], v[120:121], v[108:109] op_sel_hi:[0,1]
	v_pk_fma_f32 v[130:131], v[130:131], v[98:99], v[102:103]
	v_pk_mul_f32 v[98:99], v[120:121], v[110:111] op_sel_hi:[0,1]
	v_pk_fma_f32 v[132:133], v[132:133], v[100:101], v[98:99]
	v_pk_mul_f32 v[98:99], v[68:69], v[2:3] op_sel_hi:[0,1]
	v_exp_f32_e32 v98, v98
	v_exp_f32_e32 v99, v99
	v_pk_mul_f32 v[100:101], v[68:69], v[4:5] op_sel_hi:[0,1]
	v_exp_f32_e32 v100, v100
	v_exp_f32_e32 v101, v101
	v_pk_mul_f32 v[102:103], v[120:121], v[112:113] op_sel_hi:[0,1]
	v_pk_fma_f32 v[116:117], v[116:117], v[98:99], v[102:103]
	v_pk_mul_f32 v[98:99], v[120:121], v[114:115] op_sel_hi:[0,1]
	v_pk_fma_f32 v[118:119], v[118:119], v[100:101], v[98:99]
	s_nop 0
	s_waitcnt lgkmcnt(0)
	s_nop 0
	ds_read_b128 v[98:101], v160 offset:46640
	ds_read_b128 v[102:105], v160 offset:46656
	ds_read_b128 v[108:111], v160 offset:46672
	ds_read_b128 v[112:115], v160 offset:46688
	v_pk_mul_f32 v[134:135], v[70:71], v[14:15] op_sel_hi:[0,1]
	v_exp_f32_e32 v134, v134
	v_exp_f32_e32 v135, v135
	v_pk_mul_f32 v[136:137], v[70:71], v[16:17] op_sel_hi:[0,1]
	v_exp_f32_e32 v136, v136
	v_exp_f32_e32 v137, v137
	v_mul_f32_e32 v120, v70, v55
	v_pk_mul_f32 v[82:83], v[120:121], v[82:83] op_sel_hi:[0,1]
	v_pk_fma_f32 v[122:123], v[122:123], v[134:135], v[82:83]
	v_pk_mul_f32 v[82:83], v[120:121], v[84:85] op_sel_hi:[0,1]
	v_pk_fma_f32 v[124:125], v[124:125], v[136:137], v[82:83]
	v_pk_mul_f32 v[82:83], v[70:71], v[10:11] op_sel_hi:[0,1]
	v_exp_f32_e32 v82, v82
	v_exp_f32_e32 v83, v83
	v_pk_mul_f32 v[84:85], v[70:71], v[12:13] op_sel_hi:[0,1]
	v_exp_f32_e32 v84, v84
	v_exp_f32_e32 v85, v85
	v_pk_mul_f32 v[86:87], v[120:121], v[86:87] op_sel_hi:[0,1]
	v_pk_fma_f32 v[128:129], v[128:129], v[82:83], v[86:87]
	v_pk_mul_f32 v[82:83], v[120:121], v[88:89] op_sel_hi:[0,1]
	v_pk_fma_f32 v[126:127], v[126:127], v[84:85], v[82:83]
	v_pk_mul_f32 v[82:83], v[70:71], v[6:7] op_sel_hi:[0,1]
	v_exp_f32_e32 v82, v82
	v_exp_f32_e32 v83, v83
	v_pk_mul_f32 v[84:85], v[70:71], v[8:9] op_sel_hi:[0,1]
	v_exp_f32_e32 v84, v84
	v_exp_f32_e32 v85, v85
	v_pk_mul_f32 v[86:87], v[120:121], v[90:91] op_sel_hi:[0,1]
	v_pk_fma_f32 v[130:131], v[130:131], v[82:83], v[86:87]
	v_pk_mul_f32 v[82:83], v[120:121], v[92:93] op_sel_hi:[0,1]
	v_pk_fma_f32 v[132:133], v[132:133], v[84:85], v[82:83]
	v_pk_mul_f32 v[82:83], v[70:71], v[2:3] op_sel_hi:[0,1]
	v_exp_f32_e32 v82, v82
	v_exp_f32_e32 v83, v83
	v_pk_mul_f32 v[84:85], v[70:71], v[4:5] op_sel_hi:[0,1]
	v_exp_f32_e32 v84, v84
	v_exp_f32_e32 v85, v85
	v_pk_mul_f32 v[86:87], v[120:121], v[94:95] op_sel_hi:[0,1]
	v_pk_fma_f32 v[116:117], v[116:117], v[82:83], v[86:87]
	v_pk_mul_f32 v[82:83], v[120:121], v[96:97] op_sel_hi:[0,1]
	v_pk_fma_f32 v[118:119], v[118:119], v[84:85], v[82:83]
	s_nop 0
	s_waitcnt lgkmcnt(0)
	s_nop 0
	ds_read_b128 v[82:85], v160 offset:46848
	ds_read_b128 v[86:89], v160 offset:46864
	ds_read_b128 v[90:93], v160 offset:46880
	ds_read_b128 v[94:97], v160 offset:46896
	v_pk_mul_f32 v[134:135], v[72:73], v[14:15] op_sel_hi:[0,1]
	v_exp_f32_e32 v134, v134
	v_exp_f32_e32 v135, v135
	v_pk_mul_f32 v[136:137], v[72:73], v[16:17] op_sel_hi:[0,1]
	v_exp_f32_e32 v136, v136
	v_exp_f32_e32 v137, v137
	v_mul_f32_e32 v120, v72, v53
	v_pk_mul_f32 v[98:99], v[120:121], v[98:99] op_sel_hi:[0,1]
	v_pk_fma_f32 v[122:123], v[122:123], v[134:135], v[98:99]
	v_pk_mul_f32 v[98:99], v[120:121], v[100:101] op_sel_hi:[0,1]
	v_pk_fma_f32 v[124:125], v[124:125], v[136:137], v[98:99]
	v_pk_mul_f32 v[98:99], v[72:73], v[10:11] op_sel_hi:[0,1]
	v_exp_f32_e32 v98, v98
	v_exp_f32_e32 v99, v99
	v_pk_mul_f32 v[100:101], v[72:73], v[12:13] op_sel_hi:[0,1]
	v_exp_f32_e32 v100, v100
	v_exp_f32_e32 v101, v101
	v_pk_mul_f32 v[102:103], v[120:121], v[102:103] op_sel_hi:[0,1]
	v_pk_fma_f32 v[128:129], v[128:129], v[98:99], v[102:103]
	v_pk_mul_f32 v[98:99], v[120:121], v[104:105] op_sel_hi:[0,1]
	v_pk_fma_f32 v[126:127], v[126:127], v[100:101], v[98:99]
	v_pk_mul_f32 v[98:99], v[72:73], v[6:7] op_sel_hi:[0,1]
	v_exp_f32_e32 v98, v98
	v_exp_f32_e32 v99, v99
	v_pk_mul_f32 v[100:101], v[72:73], v[8:9] op_sel_hi:[0,1]
	v_exp_f32_e32 v100, v100
	v_exp_f32_e32 v101, v101
	v_pk_mul_f32 v[102:103], v[120:121], v[108:109] op_sel_hi:[0,1]
	v_pk_fma_f32 v[130:131], v[130:131], v[98:99], v[102:103]
	v_pk_mul_f32 v[98:99], v[120:121], v[110:111] op_sel_hi:[0,1]
	v_pk_fma_f32 v[132:133], v[132:133], v[100:101], v[98:99]
	v_pk_mul_f32 v[98:99], v[72:73], v[2:3] op_sel_hi:[0,1]
	v_exp_f32_e32 v98, v98
	v_exp_f32_e32 v99, v99
	v_pk_mul_f32 v[100:101], v[72:73], v[4:5] op_sel_hi:[0,1]
	v_exp_f32_e32 v100, v100
	v_exp_f32_e32 v101, v101
	v_pk_mul_f32 v[102:103], v[120:121], v[112:113] op_sel_hi:[0,1]
	v_pk_fma_f32 v[116:117], v[116:117], v[98:99], v[102:103]
	v_pk_mul_f32 v[98:99], v[120:121], v[114:115] op_sel_hi:[0,1]
	v_pk_fma_f32 v[118:119], v[118:119], v[100:101], v[98:99]
	s_nop 0
	s_waitcnt lgkmcnt(0)
	s_nop 0
	ds_read_b128 v[98:101], v160 offset:47056
	ds_read_b128 v[102:105], v160 offset:47072
	ds_read_b128 v[108:111], v160 offset:47088
	ds_read_b128 v[112:115], v160 offset:47104
	v_pk_mul_f32 v[134:135], v[74:75], v[14:15] op_sel_hi:[0,1]
	v_exp_f32_e32 v134, v134
	v_exp_f32_e32 v135, v135
	v_pk_mul_f32 v[136:137], v[74:75], v[16:17] op_sel_hi:[0,1]
	v_exp_f32_e32 v136, v136
	v_exp_f32_e32 v137, v137
	v_mul_f32_e32 v120, v74, v51
	v_pk_mul_f32 v[82:83], v[120:121], v[82:83] op_sel_hi:[0,1]
	v_pk_fma_f32 v[122:123], v[122:123], v[134:135], v[82:83]
	v_pk_mul_f32 v[82:83], v[120:121], v[84:85] op_sel_hi:[0,1]
	v_pk_fma_f32 v[124:125], v[124:125], v[136:137], v[82:83]
	v_pk_mul_f32 v[82:83], v[74:75], v[10:11] op_sel_hi:[0,1]
	v_exp_f32_e32 v82, v82
	v_exp_f32_e32 v83, v83
	v_pk_mul_f32 v[84:85], v[74:75], v[12:13] op_sel_hi:[0,1]
	v_exp_f32_e32 v84, v84
	v_exp_f32_e32 v85, v85
	v_pk_mul_f32 v[86:87], v[120:121], v[86:87] op_sel_hi:[0,1]
	v_pk_fma_f32 v[128:129], v[128:129], v[82:83], v[86:87]
	v_pk_mul_f32 v[82:83], v[120:121], v[88:89] op_sel_hi:[0,1]
	v_pk_fma_f32 v[126:127], v[126:127], v[84:85], v[82:83]
	v_pk_mul_f32 v[82:83], v[74:75], v[6:7] op_sel_hi:[0,1]
	v_exp_f32_e32 v82, v82
	v_exp_f32_e32 v83, v83
	v_pk_mul_f32 v[84:85], v[74:75], v[8:9] op_sel_hi:[0,1]
	v_exp_f32_e32 v84, v84
	v_exp_f32_e32 v85, v85
	v_pk_mul_f32 v[86:87], v[120:121], v[90:91] op_sel_hi:[0,1]
	v_pk_fma_f32 v[130:131], v[130:131], v[82:83], v[86:87]
	v_pk_mul_f32 v[82:83], v[120:121], v[92:93] op_sel_hi:[0,1]
	v_pk_fma_f32 v[132:133], v[132:133], v[84:85], v[82:83]
	v_pk_mul_f32 v[82:83], v[74:75], v[2:3] op_sel_hi:[0,1]
	v_exp_f32_e32 v82, v82
	v_exp_f32_e32 v83, v83
	v_pk_mul_f32 v[84:85], v[74:75], v[4:5] op_sel_hi:[0,1]
	v_exp_f32_e32 v84, v84
	v_exp_f32_e32 v85, v85
	v_pk_mul_f32 v[86:87], v[120:121], v[94:95] op_sel_hi:[0,1]
	v_pk_fma_f32 v[116:117], v[116:117], v[82:83], v[86:87]
	v_pk_mul_f32 v[82:83], v[120:121], v[96:97] op_sel_hi:[0,1]
	v_pk_fma_f32 v[118:119], v[118:119], v[84:85], v[82:83]
	s_nop 0
	s_waitcnt lgkmcnt(0)
	s_nop 0
	ds_read_b128 v[82:85], v160 offset:47264
	ds_read_b128 v[86:89], v160 offset:47280
	ds_read_b128 v[90:93], v160 offset:47296
	ds_read_b128 v[94:97], v160 offset:47312
	v_pk_mul_f32 v[134:135], v[76:77], v[14:15] op_sel_hi:[0,1]
	v_exp_f32_e32 v134, v134
	v_exp_f32_e32 v135, v135
	v_pk_mul_f32 v[136:137], v[76:77], v[16:17] op_sel_hi:[0,1]
	v_exp_f32_e32 v136, v136
	v_exp_f32_e32 v137, v137
	v_mul_f32_e32 v120, v76, v49
	v_pk_mul_f32 v[98:99], v[120:121], v[98:99] op_sel_hi:[0,1]
	v_pk_fma_f32 v[122:123], v[122:123], v[134:135], v[98:99]
	v_pk_mul_f32 v[98:99], v[120:121], v[100:101] op_sel_hi:[0,1]
	v_pk_fma_f32 v[124:125], v[124:125], v[136:137], v[98:99]
	v_pk_mul_f32 v[98:99], v[76:77], v[10:11] op_sel_hi:[0,1]
	v_exp_f32_e32 v98, v98
	v_exp_f32_e32 v99, v99
	v_pk_mul_f32 v[100:101], v[76:77], v[12:13] op_sel_hi:[0,1]
	v_exp_f32_e32 v100, v100
	v_exp_f32_e32 v101, v101
	v_pk_mul_f32 v[102:103], v[120:121], v[102:103] op_sel_hi:[0,1]
	v_pk_fma_f32 v[128:129], v[128:129], v[98:99], v[102:103]
	v_pk_mul_f32 v[98:99], v[120:121], v[104:105] op_sel_hi:[0,1]
	v_pk_fma_f32 v[126:127], v[126:127], v[100:101], v[98:99]
	v_pk_mul_f32 v[98:99], v[76:77], v[6:7] op_sel_hi:[0,1]
	v_exp_f32_e32 v98, v98
	v_exp_f32_e32 v99, v99
	v_pk_mul_f32 v[100:101], v[76:77], v[8:9] op_sel_hi:[0,1]
	v_exp_f32_e32 v100, v100
	v_exp_f32_e32 v101, v101
	v_pk_mul_f32 v[102:103], v[120:121], v[108:109] op_sel_hi:[0,1]
	v_pk_fma_f32 v[130:131], v[130:131], v[98:99], v[102:103]
	v_pk_mul_f32 v[98:99], v[120:121], v[110:111] op_sel_hi:[0,1]
	v_pk_fma_f32 v[132:133], v[132:133], v[100:101], v[98:99]
	v_pk_mul_f32 v[98:99], v[76:77], v[2:3] op_sel_hi:[0,1]
	v_exp_f32_e32 v98, v98
	v_exp_f32_e32 v99, v99
	v_pk_mul_f32 v[100:101], v[76:77], v[4:5] op_sel_hi:[0,1]
	v_exp_f32_e32 v100, v100
	v_exp_f32_e32 v101, v101
	v_pk_mul_f32 v[102:103], v[120:121], v[112:113] op_sel_hi:[0,1]
	v_pk_fma_f32 v[116:117], v[116:117], v[98:99], v[102:103]
	v_pk_mul_f32 v[98:99], v[120:121], v[114:115] op_sel_hi:[0,1]
	v_pk_fma_f32 v[118:119], v[118:119], v[100:101], v[98:99]
	s_nop 0
	s_waitcnt lgkmcnt(0)
	s_nop 0
	ds_read_b128 v[98:101], v160 offset:47472
	ds_read_b128 v[102:105], v160 offset:47488
	ds_read_b128 v[108:111], v160 offset:47504
	ds_read_b128 v[112:115], v160 offset:47520
	v_add_f32_e32 v19, 0, v80
	v_add_f32_e32 v19, v19, v20
	v_add_f32_e32 v19, v19, v22
	v_add_f32_e32 v19, v19, v24
	v_add_f32_e32 v19, v19, v26
	v_add_f32_e32 v19, v19, v28
	v_add_f32_e32 v19, v19, v30
	v_add_f32_e32 v19, v19, v32
	v_add_f32_e32 v19, v19, v34
	v_add_f32_e32 v19, v19, v36
	v_pk_mul_f32 v[134:135], v[78:79], v[14:15] op_sel_hi:[0,1]
	v_pk_mul_f32 v[136:137], v[78:79], v[16:17] op_sel_hi:[0,1]
	v_add_f32_e32 v19, v19, v38
	v_exp_f32_e32 v134, v134
	v_exp_f32_e32 v135, v135
	v_exp_f32_e32 v136, v136
	v_exp_f32_e32 v137, v137
	v_add_f32_e32 v19, v19, v40
	v_add_f32_e32 v19, v19, v42
	v_mul_f32_e32 v120, v78, v47
	v_add_f32_e32 v19, v19, v44
	v_pk_mul_f32 v[82:83], v[120:121], v[82:83] op_sel_hi:[0,1]
	v_pk_mul_f32 v[84:85], v[120:121], v[84:85] op_sel_hi:[0,1]
	v_add_f32_e32 v19, v19, v46
	v_pk_fma_f32 v[82:83], v[122:123], v[134:135], v[82:83]
	v_pk_fma_f32 v[84:85], v[124:125], v[136:137], v[84:85]
	v_pk_mul_f32 v[122:123], v[78:79], v[10:11] op_sel_hi:[0,1]
	v_pk_mul_f32 v[124:125], v[78:79], v[12:13] op_sel_hi:[0,1]
	v_add_f32_e32 v19, v19, v48
	v_exp_f32_e32 v122, v122
	v_exp_f32_e32 v123, v123
	v_exp_f32_e32 v124, v124
	v_exp_f32_e32 v125, v125
	v_add_f32_e32 v19, v19, v50
	v_add_f32_e32 v19, v19, v52
	v_add_f32_e32 v19, v19, v54
	v_pk_mul_f32 v[86:87], v[120:121], v[86:87] op_sel_hi:[0,1]
	v_pk_mul_f32 v[88:89], v[120:121], v[88:89] op_sel_hi:[0,1]
	v_add_f32_e32 v19, v19, v56
	v_pk_fma_f32 v[86:87], v[128:129], v[122:123], v[86:87]
	v_pk_fma_f32 v[88:89], v[126:127], v[124:125], v[88:89]
	v_pk_mul_f32 v[122:123], v[78:79], v[6:7] op_sel_hi:[0,1]
	v_pk_mul_f32 v[124:125], v[78:79], v[8:9] op_sel_hi:[0,1]
	v_add_f32_e32 v19, v19, v58
	v_exp_f32_e32 v122, v122
	v_exp_f32_e32 v123, v123
	v_exp_f32_e32 v124, v124
	v_exp_f32_e32 v125, v125
	v_add_f32_e32 v19, v19, v60
	v_add_f32_e32 v19, v19, v62
	v_add_f32_e32 v19, v19, v64
	v_pk_mul_f32 v[90:91], v[120:121], v[90:91] op_sel_hi:[0,1]
	v_pk_mul_f32 v[92:93], v[120:121], v[92:93] op_sel_hi:[0,1]
	v_add_f32_e32 v19, v19, v66
	v_pk_fma_f32 v[90:91], v[130:131], v[122:123], v[90:91]
	v_pk_fma_f32 v[92:93], v[132:133], v[124:125], v[92:93]
	v_pk_mul_f32 v[122:123], v[78:79], v[2:3] op_sel_hi:[0,1]
	v_pk_mul_f32 v[124:125], v[78:79], v[4:5] op_sel_hi:[0,1]
	v_add_f32_e32 v19, v19, v68
	v_exp_f32_e32 v122, v122
	v_exp_f32_e32 v123, v123
	v_exp_f32_e32 v124, v124
	v_exp_f32_e32 v125, v125
	v_add_f32_e32 v19, v19, v70
	v_add_f32_e32 v19, v19, v72
	v_add_f32_e32 v19, v19, v74
	v_pk_mul_f32 v[94:95], v[120:121], v[94:95] op_sel_hi:[0,1]
	v_pk_mul_f32 v[96:97], v[120:121], v[96:97] op_sel_hi:[0,1]
	v_add_f32_e32 v19, v19, v76
	v_pk_fma_f32 v[94:95], v[116:117], v[122:123], v[94:95]
	v_pk_fma_f32 v[96:97], v[118:119], v[124:125], v[96:97]
	v_add_f32_e32 v19, v19, v78
	s_waitcnt lgkmcnt(0)
	v_cvt_f32_f16_e32 v20, v106
	v_add_f32_e32 v19, v19, v18
	v_pk_mul_f32 v[4:5], v[18:19], v[4:5] op_sel_hi:[0,1]
	v_exp_f32_e32 v4, v4
	v_exp_f32_e32 v5, v5
	v_pk_mul_f32 v[14:15], v[18:19], v[14:15] op_sel_hi:[0,1]
	v_exp_f32_e32 v14, v14
	v_exp_f32_e32 v15, v15
	v_mul_f32_e32 v20, v18, v20
	v_pk_mul_f32 v[22:23], v[20:21], v[114:115] op_sel_hi:[0,1]
	v_pk_fma_f32 v[22:23], v[96:97], v[4:5], v[22:23]
	v_pk_mul_f32 v[4:5], v[20:21], v[98:99] op_sel_hi:[0,1]
	v_pk_fma_f32 v[14:15], v[82:83], v[14:15], v[4:5]
	v_pk_mul_f32 v[4:5], v[18:19], v[16:17] op_sel_hi:[0,1]
	v_exp_f32_e32 v4, v4
	v_exp_f32_e32 v5, v5
	v_pk_mul_f32 v[10:11], v[18:19], v[10:11] op_sel_hi:[0,1]
	v_exp_f32_e32 v10, v10
	v_exp_f32_e32 v11, v11
	v_pk_mul_f32 v[16:17], v[20:21], v[100:101] op_sel_hi:[0,1]
	v_pk_fma_f32 v[16:17], v[84:85], v[4:5], v[16:17]
	v_pk_mul_f32 v[4:5], v[20:21], v[102:103] op_sel_hi:[0,1]
	v_pk_fma_f32 v[10:11], v[86:87], v[10:11], v[4:5]
	v_pk_mul_f32 v[4:5], v[18:19], v[12:13] op_sel_hi:[0,1]
	v_exp_f32_e32 v4, v4
	v_exp_f32_e32 v5, v5
	v_pk_mul_f32 v[6:7], v[18:19], v[6:7] op_sel_hi:[0,1]
	v_exp_f32_e32 v6, v6
	v_exp_f32_e32 v7, v7
	v_pk_mul_f32 v[8:9], v[18:19], v[8:9] op_sel_hi:[0,1]
	v_exp_f32_e32 v8, v8
	v_exp_f32_e32 v9, v9
	v_pk_mul_f32 v[2:3], v[18:19], v[2:3] op_sel_hi:[0,1]
	v_pk_mul_f32 v[12:13], v[20:21], v[104:105] op_sel_hi:[0,1]
	v_exp_f32_e32 v2, v2
	v_exp_f32_e32 v3, v3
	v_pk_fma_f32 v[4:5], v[88:89], v[4:5], v[12:13]
	v_pk_mul_f32 v[12:13], v[20:21], v[108:109] op_sel_hi:[0,1]
	v_pk_fma_f32 v[6:7], v[90:91], v[6:7], v[12:13]
	v_pk_mul_f32 v[12:13], v[20:21], v[110:111] op_sel_hi:[0,1]
	v_pk_fma_f32 v[8:9], v[92:93], v[8:9], v[12:13]
	v_pk_mul_f32 v[12:13], v[20:21], v[112:113] op_sel_hi:[0,1]
	v_cvt_pk_f16_f32 v5, v4, v5
	v_cvt_pk_f16_f32 v4, v10, v11
	v_lshl_or_b32 v10, v0, 4, s6
	v_mov_b32_e32 v11, s7
	v_pk_fma_f32 v[12:13], v[94:95], v[2:3], v[12:13]
	v_cvt_pk_f16_f32 v3, v16, v17
	v_cvt_pk_f16_f32 v2, v14, v15
	v_lshl_add_u64 v[10:11], s[4:5], 0, v[10:11]
	s_movk_i32 s4, 0x2000
	global_store_dwordx4 v[10:11], v[2:5], off sc0 sc1
	global_store_dword v1, v19, s[0:1] sc0 sc1
	s_nop 0
	v_cvt_pk_f16_f32 v2, v6, v7
	v_add_co_u32_e32 v6, vcc, s4, v10
	v_cvt_pk_f16_f32 v5, v22, v23
	v_cvt_pk_f16_f32 v4, v12, v13
	v_cvt_pk_f16_f32 v3, v8, v9
	v_addc_co_u32_e32 v7, vcc, 0, v11, vcc
	global_store_dwordx4 v[6:7], v[2:5], off sc0 sc1
	s_endpgm

	.amdhsa_kernel _Z12k_conv_xprojPKDF16_PKfS2_S0_S0_S2_PDF16_S3_PfS2_S3_S4_
		.amdhsa_group_segment_fixed_size 47616
		.amdhsa_private_segment_fixed_size 0
		.amdhsa_kernarg_size 96
		.amdhsa_user_sgpr_count 2
		.amdhsa_user_sgpr_dispatch_ptr 0
		.amdhsa_user_sgpr_queue_ptr 0
		.amdhsa_user_sgpr_kernarg_segment_ptr 1
		.amdhsa_user_sgpr_dispatch_id 0
		.amdhsa_user_sgpr_kernarg_preload_length 0
		.amdhsa_user_sgpr_kernarg_preload_offset 0
		.amdhsa_user_sgpr_private_segment_size 0
		.amdhsa_uses_dynamic_stack 0
		.amdhsa_enable_private_segment 0
		.amdhsa_system_sgpr_workgroup_id_x 1
		.amdhsa_system_sgpr_workgroup_id_y 0
		.amdhsa_system_sgpr_workgroup_id_z 0
		.amdhsa_system_sgpr_workgroup_info 0
		.amdhsa_system_vgpr_workitem_id 0
		.amdhsa_next_free_vgpr 232
		.amdhsa_next_free_sgpr 91
		.amdhsa_accum_offset 232
		.amdhsa_reserve_vcc 1
		.amdhsa_float_round_mode_32 0
		.amdhsa_float_round_mode_16_64 0
		.amdhsa_float_denorm_mode_32 3
		.amdhsa_float_denorm_mode_16_64 3
		.amdhsa_dx10_clamp 1
		.amdhsa_ieee_mode 1
		.amdhsa_fp16_overflow 0
		.amdhsa_tg_split 0
		.amdhsa_exception_fp_ieee_invalid_op 0
		.amdhsa_exception_fp_denorm_src 0
		.amdhsa_exception_fp_ieee_div_zero 0
		.amdhsa_exception_fp_ieee_overflow 0
		.amdhsa_exception_fp_ieee_underflow 0
		.amdhsa_exception_fp_ieee_inexact 0
		.amdhsa_exception_int_div_zero 0
	.end_amdhsa_kernel

amdhsa.kernels:
  - .agpr_count:     0
    .args:
      - .actual_access:  read_only
        .address_space:  global
        .offset:         0
        .size:           8
        .value_kind:     global_buffer
      - .actual_access:  write_only
        .address_space:  global
        .offset:         8
        .size:           8
        .value_kind:     global_buffer
      - .offset:         16
        .size:           4
        .value_kind:     by_value
      - .offset:         20
        .size:           4
        .value_kind:     by_value
      - .actual_access:  read_only
        .address_space:  global
        .offset:         24
        .size:           8
        .value_kind:     global_buffer
      - .actual_access:  write_only
        .address_space:  global
        .offset:         32
        .size:           8
        .value_kind:     global_buffer
      - .offset:         40
        .size:           4
        .value_kind:     by_value
      - .offset:         44
        .size:           4
        .value_kind:     by_value
      - .actual_access:  read_only
        .address_space:  global
        .offset:         48
        .size:           8
        .value_kind:     global_buffer
      - .actual_access:  write_only
        .address_space:  global
        .offset:         56
        .size:           8
        .value_kind:     global_buffer
      - .offset:         64
        .size:           4
        .value_kind:     by_value
      - .offset:         68
        .size:           4
        .value_kind:     by_value
      - .actual_access:  read_only
        .address_space:  global
        .offset:         72
        .size:           8
        .value_kind:     global_buffer
      - .actual_access:  write_only
        .address_space:  global
        .offset:         80
        .size:           8
        .value_kind:     global_buffer
      - .offset:         88
        .size:           4
        .value_kind:     by_value
      - .actual_access:  read_only
        .address_space:  global
        .offset:         96
        .size:           8
        .value_kind:     global_buffer
      - .actual_access:  write_only
        .address_space:  global
        .offset:         104
        .size:           8
        .value_kind:     global_buffer
      - .offset:         112
        .size:           4
        .value_kind:     by_value
      - .offset:         120
        .size:           4
        .value_kind:     hidden_block_count_x
      - .offset:         124
        .size:           4
        .value_kind:     hidden_block_count_y
      - .offset:         128
        .size:           4
        .value_kind:     hidden_block_count_z
      - .offset:         132
        .size:           2
        .value_kind:     hidden_group_size_x
      - .offset:         134
        .size:           2
        .value_kind:     hidden_group_size_y
      - .offset:         136
        .size:           2
        .value_kind:     hidden_group_size_z
      - .offset:         138
        .size:           2
        .value_kind:     hidden_remainder_x
      - .offset:         140
        .size:           2
        .value_kind:     hidden_remainder_y
      - .offset:         142
        .size:           2
        .value_kind:     hidden_remainder_z
      - .offset:         160
        .size:           8
        .value_kind:     hidden_global_offset_x
      - .offset:         168
        .size:           8
        .value_kind:     hidden_global_offset_y
      - .offset:         176
        .size:           8
        .value_kind:     hidden_global_offset_z
      - .offset:         184
        .size:           2
        .value_kind:     hidden_grid_dims
    .group_segment_fixed_size: 0
    .kernarg_segment_align: 8
    .kernarg_segment_size: 376
    .language:       OpenCL C
    .language_version:
      - 2
      - 0
    .max_flat_workgroup_size: 1024
    .name:           _Z5k_swzPKfPDF16_iiS0_S1_iiS0_S1_iiS0_PfiS0_S1_i
    .private_segment_fixed_size: 0
    .sgpr_count:     32
    .sgpr_spill_count: 0
    .symbol:         _Z5k_swzPKfPDF16_iiS0_S1_iiS0_S1_iiS0_PfiS0_S1_i.kd
    .uniform_work_group_size: 1
    .uses_dynamic_stack: false
    .vgpr_count:     14
    .vgpr_spill_count: 0
    .wavefront_size: 64
  - .agpr_count:     0
    .args:
      - .actual_access:  read_only
        .address_space:  global
        .offset:         0
        .size:           8
        .value_kind:     global_buffer
      - .actual_access:  read_only
        .address_space:  global
        .offset:         8
        .size:           8
        .value_kind:     global_buffer
      - .actual_access:  write_only
        .address_space:  global
        .offset:         16
        .size:           8
        .value_kind:     global_buffer
      - .actual_access:  read_only
        .address_space:  global
        .offset:         24
        .size:           8
        .value_kind:     global_buffer
      - .actual_access:  read_only
        .address_space:  global
        .offset:         32
        .size:           8
        .value_kind:     global_buffer
      - .actual_access:  read_only
        .address_space:  global
        .offset:         40
        .size:           8
        .value_kind:     global_buffer
      - .actual_access:  write_only
        .address_space:  global
        .offset:         48
        .size:           8
        .value_kind:     global_buffer
    .group_segment_fixed_size: 98816
    .kernarg_segment_align: 8
    .kernarg_segment_size: 56
    .language:       OpenCL C
    .language_version:
      - 2
      - 0
    .max_flat_workgroup_size: 512
    .name:           _Z10k_ka_firstPKfPKiPfS0_S0_PKDF16_PDF16_
    .private_segment_fixed_size: 0
    .sgpr_count:     59
    .sgpr_spill_count: 0
    .symbol:         _Z10k_ka_firstPKfPKiPfS0_S0_PKDF16_PDF16_.kd
    .uniform_work_group_size: 1
    .uses_dynamic_stack: false
    .vgpr_count:     174
    .vgpr_spill_count: 0
    .wavefront_size: 64
  - .agpr_count:     0
    .args:
      - .actual_access:  read_only
        .address_space:  global
        .offset:         0
        .size:           8
        .value_kind:     global_buffer
      - .actual_access:  read_only
        .address_space:  global
        .offset:         8
        .size:           8
        .value_kind:     global_buffer
      - .actual_access:  read_only
        .address_space:  global
        .offset:         16
        .size:           8
        .value_kind:     global_buffer
      - .actual_access:  read_only
        .address_space:  global
        .offset:         24
        .size:           8
        .value_kind:     global_buffer
      - .actual_access:  read_only
        .address_space:  global
        .offset:         32
        .size:           8
        .value_kind:     global_buffer
      - .actual_access:  read_only
        .address_space:  global
        .offset:         40
        .size:           8
        .value_kind:     global_buffer
      - .actual_access:  write_only
        .address_space:  global
        .offset:         48
        .size:           8
        .value_kind:     global_buffer
      - .actual_access:  write_only
        .address_space:  global
        .offset:         56
        .size:           8
        .value_kind:     global_buffer
      - .actual_access:  write_only
        .address_space:  global
        .offset:         64
        .size:           8
        .value_kind:     global_buffer
      - .actual_access:  read_only
        .address_space:  global
        .offset:         72
        .size:           8
        .value_kind:     global_buffer
      - .actual_access:  write_only
        .address_space:  global
        .offset:         80
        .size:           8
        .value_kind:     global_buffer
      - .actual_access:  write_only
        .address_space:  global
        .offset:         88
        .size:           8
        .value_kind:     global_buffer
    .group_segment_fixed_size: 47616
    .kernarg_segment_align: 8
    .kernarg_segment_size: 96
    .language:       OpenCL C
    .language_version:
      - 2
      - 0
    .max_flat_workgroup_size: 512
    .name:           _Z12k_conv_xprojPKDF16_PKfS2_S0_S0_S2_PDF16_S3_PfS2_S3_S4_
    .private_segment_fixed_size: 0
    .sgpr_count:     32
    .sgpr_spill_count: 0
    .symbol:         _Z12k_conv_xprojPKDF16_PKfS2_S0_S0_S2_PDF16_S3_PfS2_S3_S4_.kd
    .uniform_work_group_size: 1
    .uses_dynamic_stack: false
    .vgpr_count:     232
    .vgpr_spill_count: 0
    .wavefront_size: 64
  - .agpr_count:     0
    .args:
      - .actual_access:  read_only
        .address_space:  global
        .offset:         0
        .size:           8
        .value_kind:     global_buffer
      - .actual_access:  read_only
        .address_space:  global
        .offset:         8
        .size:           8
        .value_kind:     global_buffer
      - .actual_access:  read_only
        .address_space:  global
        .offset:         16
        .size:           8
        .value_kind:     global_buffer
      - .actual_access:  write_only
        .address_space:  global
        .offset:         24
        .size:           8
        .value_kind:     global_buffer
    .group_segment_fixed_size: 16384
    .kernarg_segment_align: 8
    .kernarg_segment_size: 32
    .language:       OpenCL C
    .language_version:
      - 2
      - 0
    .max_flat_workgroup_size: 512
    .name:           _Z11k_scan_combPKDF16_PKfS2_PDF16_
    .private_segment_fixed_size: 0
    .sgpr_count:     18
    .sgpr_spill_count: 0
    .symbol:         _Z11k_scan_combPKDF16_PKfS2_PDF16_.kd
    .uniform_work_group_size: 1
    .uses_dynamic_stack: false
    .vgpr_count:     120
    .vgpr_spill_count: 0
    .wavefront_size: 64
  - .agpr_count:     0
    .args:
      - .actual_access:  read_only
        .address_space:  global
        .offset:         0
        .size:           8
        .value_kind:     global_buffer
      - .actual_access:  read_only
        .address_space:  global
        .offset:         8
        .size:           8
        .value_kind:     global_buffer
      - .actual_access:  read_only
        .address_space:  global
        .offset:         16
        .size:           8
        .value_kind:     global_buffer
      - .actual_access:  read_only
        .address_space:  global
        .offset:         24
        .size:           8
        .value_kind:     global_buffer
      - .actual_access:  write_only
        .address_space:  global
        .offset:         32
        .size:           8
        .value_kind:     global_buffer
    .group_segment_fixed_size: 32
    .kernarg_segment_align: 8
    .kernarg_segment_size: 40
    .language:       OpenCL C
    .language_version:
      - 2
      - 0
    .max_flat_workgroup_size: 256
    .name:           _Z6k_headPKfS0_S0_S0_Pf
    .private_segment_fixed_size: 0
    .sgpr_count:     86
    .sgpr_spill_count: 0
    .symbol:         _Z6k_headPKfS0_S0_S0_Pf.kd
    .uniform_work_group_size: 1
    .uses_dynamic_stack: false
    .vgpr_count:     92
    .vgpr_spill_count: 0
    .wavefront_size: 64
  - .agpr_count:     0
    .args:
      - .actual_access:  read_only
        .address_space:  global
        .offset:         0
        .size:           8
        .value_kind:     global_buffer
      - .actual_access:  read_only
        .address_space:  global
        .offset:         8
        .size:           8
        .value_kind:     global_buffer
      - .actual_access:  read_only
        .address_space:  global
        .offset:         16
        .size:           8
        .value_kind:     global_buffer
      - .actual_access:  read_only
        .address_space:  global
        .offset:         24
        .size:           8
        .value_kind:     global_buffer
      - .actual_access:  read_only
        .address_space:  global
        .offset:         32
        .size:           8
        .value_kind:     global_buffer
      - .actual_access:  read_only
        .address_space:  global
        .offset:         40
        .size:           8
        .value_kind:     global_buffer
      - .actual_access:  read_only
        .address_space:  global
        .offset:         48
        .size:           8
        .value_kind:     global_buffer
      - .address_space:  global
        .offset:         56
        .size:           8
        .value_kind:     global_buffer
      - .actual_access:  read_only
        .address_space:  global
        .offset:         64
        .size:           8
        .value_kind:     global_buffer
      - .actual_access:  read_only
        .address_space:  global
        .offset:         72
        .size:           8
        .value_kind:     global_buffer
      - .actual_access:  read_only
        .address_space:  global
        .offset:         80
        .size:           8
        .value_kind:     global_buffer
      - .address_space:  global
        .offset:         88
        .size:           8
        .value_kind:     global_buffer
      - .actual_access:  read_only
        .address_space:  global
        .offset:         96
        .size:           8
        .value_kind:     global_buffer
      - .actual_access:  read_only
        .address_space:  global
        .offset:         104
        .size:           8
        .value_kind:     global_buffer
      - .actual_access:  read_only
        .address_space:  global
        .offset:         112
        .size:           8
        .value_kind:     global_buffer
    .group_segment_fixed_size: 98816
    .kernarg_segment_align: 8
    .kernarg_segment_size: 120
    .language:       OpenCL C
    .language_version:
      - 2
      - 0
    .max_flat_workgroup_size: 512
    .name:           _Z4k_k2ILb0EEvPKDF16_S1_PKfS3_S3_S1_S1_PfS3_S3_S1_PDF16_PKiS4_S4_
    .private_segment_fixed_size: 0
    .sgpr_count:     106
    .sgpr_spill_count: 0
    .symbol:         _Z4k_k2ILb0EEvPKDF16_S1_PKfS3_S3_S1_S1_PfS3_S3_S1_PDF16_PKiS4_S4_.kd
    .uniform_work_group_size: 1
    .uses_dynamic_stack: false
    .vgpr_count:     232
    .vgpr_spill_count: 0
    .wavefront_size: 64
  - .agpr_count:     0
    .args:
      - .actual_access:  read_only
        .address_space:  global
        .offset:         0
        .size:           8
        .value_kind:     global_buffer
      - .actual_access:  read_only
        .address_space:  global
        .offset:         8
        .size:           8
        .value_kind:     global_buffer
      - .actual_access:  read_only
        .address_space:  global
        .offset:         16
        .size:           8
        .value_kind:     global_buffer
      - .actual_access:  read_only
        .address_space:  global
        .offset:         24
        .size:           8
        .value_kind:     global_buffer
      - .actual_access:  read_only
        .address_space:  global
        .offset:         32
        .size:           8
        .value_kind:     global_buffer
      - .actual_access:  read_only
        .address_space:  global
        .offset:         40
        .size:           8
        .value_kind:     global_buffer
      - .actual_access:  read_only
        .address_space:  global
        .offset:         48
        .size:           8
        .value_kind:     global_buffer
      - .actual_access:  read_only
        .address_space:  global
        .offset:         56
        .size:           8
        .value_kind:     global_buffer
      - .actual_access:  read_only
        .address_space:  global
        .offset:         64
        .size:           8
        .value_kind:     global_buffer
      - .actual_access:  read_only
        .address_space:  global
        .offset:         72
        .size:           8
        .value_kind:     global_buffer
      - .actual_access:  read_only
        .address_space:  global
        .offset:         80
        .size:           8
        .value_kind:     global_buffer
      - .actual_access:  read_only
        .address_space:  global
        .offset:         88
        .size:           8
        .value_kind:     global_buffer
      - .actual_access:  read_only
        .address_space:  global
        .offset:         96
        .size:           8
        .value_kind:     global_buffer
      - .actual_access:  write_only
        .address_space:  global
        .offset:         104
        .size:           8
        .value_kind:     global_buffer
      - .actual_access:  write_only
        .address_space:  global
        .offset:         112
        .size:           8
        .value_kind:     global_buffer
    .group_segment_fixed_size: 98816
    .kernarg_segment_align: 8
    .kernarg_segment_size: 120
    .language:       OpenCL C
    .language_version:
      - 2
      - 0
    .max_flat_workgroup_size: 512
    .name:           _Z4k_k2ILb1EEvPKDF16_S1_PKfS3_S3_S1_S1_PfS3_S3_S1_PDF16_PKiS4_S4_
    .private_segment_fixed_size: 0
    .sgpr_count:     44
    .sgpr_spill_count: 0
    .symbol:         _Z4k_k2ILb1EEvPKDF16_S1_PKfS3_S3_S1_S1_PfS3_S3_S1_PDF16_PKiS4_S4_.kd
    .uniform_work_group_size: 1
    .uses_dynamic_stack: false
    .vgpr_count:     196
    .vgpr_spill_count: 0
    .wavefront_size: 64
